# stack: barrier polls cross-XCC generation directly; MoE1 padding-only waves skip MFMAs; odd WGs run LRU output units before mLSTM unit in phase 3
# speedup vs baseline: 1.0436x; 1.0067x over previous
; __device__ __forceinline__ unsigned xb_ld(unsigned* p)              { return __hip_atomic_load(p, __ATOMIC_RELAXED, __HIP_MEMORY_SCOPE_AGENT); }
; __device__ __forceinline__ unsigned xb_add(unsigned* p, unsigned v) { return __hip_atomic_fetch_add(p, v, __ATOMIC_RELAXED, __HIP_MEMORY_SCOPE_AGENT); }
; #define XB_SPIN(cond, bar) do { unsigned _sp = 0; while (cond) { __builtin_amdgcn_s_sleep(1); \
;     if ((++_sp & 255u) == 0u) { if (xb_ld(&(bar)[XB_TMO])) break; if (_sp > XB_SPIN_CAP) { atomicAdd(&(bar)[XB_TMO], 1u); break; } } } } while (0)
; __device__ __forceinline__ void xcd_barrier(const XcdBarrier& b, int tid) {
;     ...
;         const unsigned old = xb_add(&bar[XB_XSUB(b.x)], 1u);
;         const unsigned gen = old / nloc;
;         if (old + 1u == (gen + 1u) * nloc) {
;             __builtin_amdgcn_fence(__ATOMIC_RELEASE, "agent");
;             asm volatile("s_waitcnt vmcnt(0)" ::: "memory");
;             const unsigned og = xb_add(&bar[XB_TOP], 1u);
;             const unsigned tg = og / nx;
;             if (og + 1u == (tg + 1u) * nx) xb_add(&bar[XB_TOPGEN], 1u);
;             else XB_SPIN(xb_ld(&bar[XB_TOPGEN]) == tg, bar);
;             __builtin_amdgcn_fence(__ATOMIC_ACQUIRE, "agent");
;             xb_add(&bar[XB_XGEN(b.x)], 1u);
;             asm volatile("s_waitcnt vmcnt(0)" ::: "memory");
;         } else {
;             XB_SPIN(xb_ld(&bar[XB_XGEN(b.x)]) == gen, bar);
;             __builtin_amdgcn_fence(__ATOMIC_ACQUIRE, "agent");
;             asm volatile("s_waitcnt vmcnt(0)" ::: "memory");
;         }
.LBB0_105:
	v_readlane_b32 s0, v249, 2
	s_lshl_b32 s0, s0, 8
	v_readlane_b32 s2, v249, 3
	v_readlane_b32 s3, v249, 4
	s_add_u32 s8, s2, s0
	s_addc_u32 s9, s3, 0
	v_mov_b32_e32 v1, 0x1000
	v_mov_b32_e32 v3, 1
	global_atomic_add v3, v1, v3, s[8:9] offset:1024 sc0
	v_cvt_f32_u32_e32 v1, v2
	v_sub_u32_e32 v4, 0, v2
	v_rcp_iflag_f32_e32 v1, v1
	s_nop 0
	v_mul_f32_e32 v1, 0x4f7ffffe, v1
	v_cvt_u32_f32_e32 v1, v1
	v_mul_lo_u32 v4, v4, v1
	v_mul_hi_u32 v4, v1, v4
	v_add_u32_e32 v1, v1, v4
	s_waitcnt vmcnt(0)
	v_mul_hi_u32 v1, v3, v1
	v_mul_lo_u32 v4, v1, v2
	v_sub_u32_e32 v4, v3, v4
	v_add_u32_e32 v5, 1, v1
	v_cmp_ge_u32_e32 vcc, v4, v2
	v_add_u32_e32 v3, 1, v3
	s_nop 0
	v_cndmask_b32_e32 v1, v1, v5, vcc
	v_sub_u32_e32 v5, v4, v2
	v_cndmask_b32_e32 v4, v4, v5, vcc
	v_add_u32_e32 v5, 1, v1
	v_cmp_ge_u32_e32 vcc, v4, v2
	s_nop 1
	v_cndmask_b32_e32 v1, v1, v5, vcc
	v_mul_lo_u32 v4, v2, v1
	v_add_u32_e32 v2, v4, v2
	v_cmp_ne_u32_e32 vcc, v3, v2
	s_and_saveexec_b64 s[0:1], vcc
	s_xor_b64 s[10:11], exec, s[0:1]
	s_cbranch_execz .LBB0_119
	s_waitcnt lgkmcnt(0)
	buffer_inv sc1
	v_mov_b32_e32 v0, 0x7100
	global_load_dword v0, v0, s[84:85] offset:1024 sc1
	s_add_u32 s16, s84, 0x7500
	s_addc_u32 s17, s85, 0
	s_waitcnt vmcnt(0)
	v_cmp_eq_u32_e32 vcc, v0, v1
	s_and_saveexec_b64 s[12:13], vcc
	s_cbranch_execz .LBB0_118
	s_add_u32 s14, s84, 0x4200
	s_addc_u32 s15, s85, 0
	s_mov_b32 s2, 1
	s_mov_b64 s[18:19], 0
	v_mov_b32_e32 v0, 0
	s_branch .LBB0_109

; __device__ __forceinline__ int fresh_lane() { int l; asm volatile("v_mbcnt_lo_u32_b32 %0, -1, 0\n\tv_mbcnt_hi_u32_b32 %0, -1, %0" : "=v"(l)); __builtin_assume(l >= 0 && l < 64); return l; }
; #define FRESH() const int tid = TID(), lane = tid & 63, wave = __builtin_amdgcn_readfirstlane(tid >> 6); (void)lane; (void)wave
; #define PH(k, ...) if (IN(k)) { _Pragma("unroll") for (int rep_ = 0; rep_ < ((DUP_PHASE) == (k) ? 2 : 1); ++rep_) { if (rep_) xcd_barrier(bar, TID()); __VA_ARGS__ } } SEAM(k);
; __device__ __forceinline__ void ml_out_unit(const Args& a, unsigned char* lds_g, int u, int tid) {
;     const int L = u & 7, h = (u >> 3) & 7, b = u >> 6;
;     const int rowbase = NCTX + b * SEQ + 256 * L;
;     const int lane = tid & 63, w = __builtin_amdgcn_readfirstlane(tid >> 6), fr = lane & 15, fq = lane >> 4;
;     bf16* CB = (bf16*)(lds_g + ML_CB);
;     ml_gates(a, lds_g, rowbase, h, tid);
; __global__ void __launch_bounds__(NTHR, 2) fwd_kernel(Args args) {
;     ...
;     PH(3, { FRESH();
;         for (int u = c; u < 256; u += G) ml_out_unit(args, lds, u, tid);
;         unsigned psw[2][16];
;         if (c < 4 * 32 * 8) { const int q = c >> 3; lru_out_loadps(args, q >> 5, 4 + (q & 31), c & 7, __builtin_amdgcn_readfirstlane(tid >> 6) * 64 + fresh_lane(), psw); }
.LBB0_365:
	s_cmp_lt_i32 s86, 4
	s_cselect_b64 s[0:1], -1, 0
	s_and_b64 s[0:1], s[0:1], s[4:5]
	s_andn2_b64 vcc, exec, s[0:1]
	s_cbranch_vccnz .LBB0_685
	v_writelane_b32 v249, s0, 24
	s_nop 0
	v_writelane_b32 v249, s1, 25
	v_mbcnt_lo_u32_b32 v4, -1, 0
	v_mbcnt_hi_u32_b32 v4, -1, v4
	v_readlane_b32 s0, v249, 1
	s_nop 1
	v_or_b32_e32 v113, s0, v4
	s_mov_b32 s100, 0
	s_bitcmp1_b32 s83, 0
	s_cbranch_scc0 .Lp3_ml
	s_mov_b32 s100, 1
	s_branch .LBB0_667
.Lp3_ml:
	s_cmpk_gt_i32 s83, 0xff
	v_mbcnt_lo_u32_b32 v4, -1, 0
	v_mbcnt_hi_u32_b32 v4, -1, v4
	s_nop 0
	s_nop 0
	s_nop 0
	v_readlane_b32 s0, v249, 1
	s_nop 1
	v_or_b32_e32 v113, s0, v4
	s_cbranch_scc1 .LBB0_667
	s_add_u32 s0, s84, 0x200000
	s_addc_u32 s1, s85, 0
	v_writelane_b32 v249, s0, 26
	v_lshlrev_b32_e32 v10, 3, v4
	v_and_b32_e32 v10, 24, v10
	v_writelane_b32 v249, s1, 27
	s_add_u32 s0, s84, 0x3d600000
	v_writelane_b32 v249, s0, 28
	s_addc_u32 s0, s85, 0
	s_add_u32 s72, s84, 0x1ec00000
	s_addc_u32 s73, s85, 0
	s_add_u32 s46, s84, 0x22200000
	s_addc_u32 s47, s85, 0
	s_add_u32 s2, s84, 0x1fe00000
	s_addc_u32 s3, s85, 0
	s_add_u32 s54, s84, 0x37200000
	s_addc_u32 s55, s85, 0
	s_waitcnt lgkmcnt(0)
	s_add_u32 s56, s84, 0x24200000
	s_addc_u32 s57, s85, 0
	v_writelane_b32 v249, s0, 29
	s_add_u32 s0, s84, 0x3b200000
	v_lshrrev_b32_e32 v133, 3, v113
	v_add_u32_e32 v149, 0, v10
	v_lshrrev_b32_e32 v10, 1, v4
	v_writelane_b32 v249, s0, 30
	s_addc_u32 s0, s85, 0
	v_and_b32_e32 v112, 15, v4
	v_lshrrev_b32_e32 v1, 2, v113
	v_lshrrev_b32_e32 v0, 1, v113
	v_and_b32_e32 v7, 7, v4
	v_mul_u32_u24_e32 v2, 0x88, v133
	v_and_b32_e32 v10, 24, v10
	v_writelane_b32 v249, s0, 31
	v_mov_b32_e32 v5, 0
	v_and_b32_e32 v3, 24, v0
	v_lshrrev_b32_e32 v6, 4, v4
	v_lshlrev_b32_e32 v0, 4, v7
	v_lshl_add_u32 v8, v2, 1, 0
	v_lshlrev_b32_e32 v2, 5, v7
	v_cmp_eq_u32_e64 s[36:37], 0, v7
	v_lshrrev_b32_e32 v7, 2, v4
	s_add_i32 s1, 0, 0x17d40
	v_and_or_b32 v1, v1, 3, v10
	s_movk_i32 s50, 0x110
	v_mul_u32_u24_e32 v10, 0x110, v112
	v_lshlrev_b32_e32 v135, 2, v6
	s_movk_i32 s0, 0x88
	v_and_b32_e32 v150, -16, v4
	v_writelane_b32 v249, s1, 32
	v_lshlrev_b32_e32 v6, 3, v6
	v_mad_u32_u24 v153, v7, s50, v149
	v_lshlrev_b32_e32 v154, 5, v7
	v_mov_b32_e32 v7, 0x1100
	v_add3_u32 v162, 0, v3, v10
	v_mov_b32_e32 v3, v5
	v_add_u32_e32 v146, v8, v2
	v_add_u32_e32 v151, s1, v150
	v_mad_u32_u24 v159, v1, s0, v7
	v_add3_u32 v161, 0, v6, v10
	v_lshl_add_u64 v[6:7], v[4:5], 3, s[84:85]
	s_mov_b64 s[0:1], 0x3d800000
	v_lshl_add_u64 v[116:117], s[72:73], 0, v[2:3]
	v_writelane_b32 v249, s2, 33
	v_lshl_add_u64 v[114:115], v[6:7], 0, s[0:1]
	s_mov_b64 s[0:1], 0x23200000
	v_lshl_add_u64 v[118:119], s[2:3], 0, v[2:3]
	v_lshlrev_b32_e32 v2, 1, v112
	v_writelane_b32 v249, s3, 34
	v_lshl_add_u64 v[2:3], s[84:85], 0, v[2:3]
	v_cmp_eq_u32_e64 s[4:5], 0, v112
	v_lshl_add_u64 v[120:121], v[2:3], 0, s[0:1]
	v_readlane_b32 s0, v249, 1
	v_and_b32_e32 v147, 48, v4
	v_add_u32_e32 v148, 0, v147
	v_add_u32_e32 v2, s0, v4
	s_xor_b64 s[0:1], s[4:5], -1
	v_writelane_b32 v249, s0, 35
	v_lshrrev_b32_e32 v2, 3, v2
	v_or_b32_e32 v11, 1, v135
	v_writelane_b32 v249, s1, 36
	v_lshlrev_b32_e32 v158, 5, v1
	v_lshlrev_b32_e32 v3, 2, v2
	v_lshlrev_b32_e32 v122, 1, v0
	v_mbcnt_lo_u32_b32 v0, -1, 0
	v_writelane_b32 v249, s96, 37
	v_mul_i32_i24_e32 v9, 0xffffff10, v133
	v_mad_u32_u24 v152, v112, s50, v148
	v_cmp_lt_u32_e64 s[8:9], v11, v112
	v_or_b32_e32 v11, 2, v135
	v_or_b32_e32 v12, 3, v135
	v_mul_u32_u24_e32 v156, 0x88, v1
	v_or_b32_e32 v1, 0x400, v158
	v_add_u32_e32 v4, 0, v3
	s_mov_b32 s62, 0xffe00000
	v_mbcnt_hi_u32_b32 v173, -1, v0
	v_mov_b32_e32 v0, 0x80
	v_writelane_b32 v249, s97, 38
	s_mov_b32 s61, 0
	v_cmp_lt_u32_e64 s[6:7], v135, v112
	v_cmp_lt_u32_e64 s[10:11], v11, v112
	v_cmp_lt_u32_e64 s[12:13], v12, v112
	v_add_u32_e32 v155, 0xd400, v152
	v_lshl_add_u32 v157, v156, 1, v149
	v_lshl_add_u32 v160, v159, 1, v149
	v_cmp_gt_u32_e64 s[14:15], v135, v112
	v_cmp_gt_u32_e64 s[16:17], v11, v112
	v_cmp_gt_u32_e64 s[18:19], v12, v112
	v_add_u32_e32 v163, 0, v150
	v_add_u32_e32 v164, 0x440, v2
	v_add_u32_e32 v165, 0x17500, v4
	v_add_u32_e32 v166, 0x480, v2
	v_add_u32_e32 v167, 0x17c00, v3
	v_mov_b32_e32 v168, 0x3ecc95a3
	v_mov_b32_e32 v169, 0x7f800000
	s_movk_i32 s49, 0x1000
	s_mov_b32 s63, -1
	s_add_i32 s2, 0, 0x17e40
	s_movk_i32 s51, 0x7fff
	v_mov_b32_e32 v170, 0x358637bd
	v_mov_b32_e32 v171, 0x7fc00000
	v_mov_b32_e32 v172, 0xff800000
	v_lshl_or_b32 v174, v173, 2, v0
	v_mov_b32_e32 v175, 0x1200
	v_add_u32_e32 v176, v8, v9
	v_mov_b32_e32 v8, v5
	v_mov_b32_e32 v9, v5
	v_mov_b32_e32 v10, v5
	v_mov_b32_e32 v11, v5
	v_add_u32_e32 v177, v149, v1
	s_mov_b32 s3, s83
	s_mov_b32 s0, s83
	v_writelane_b32 v249, s83, 39
	v_writelane_b32 v249, s82, 40
	s_branch .LBB0_369

; __device__ __forceinline__ int fresh_lane() { int l; asm volatile("v_mbcnt_lo_u32_b32 %0, -1, 0\n\tv_mbcnt_hi_u32_b32 %0, -1, %0" : "=v"(l)); __builtin_assume(l >= 0 && l < 64); return l; }
; __device__ __forceinline__ void lru_out_loadps(const Args& a, int b, int cidx, int blk, int tid, unsigned (&psw)[2][16]) {
;     const int chl = tid & 127, q = tid >> 7, ch = blk * 128 + chl;
; #pragma unroll
;     for (int d = 0; d < 2; ++d) { const unsigned* PS = (const unsigned*)(a.ws + WS_PS) + ((size_t)(b * 2 + d) * NSTEP + 64 * cidx + 16 * q) * 1024 + ch;
; #pragma unroll
;         for (int i = 0; i < 16; ++i) psw[d][i] = PS[(size_t)i * 1024]; }
; }
; __global__ void __launch_bounds__(NTHR, 2) fwd_kernel(Args args) {
;     ...
;         if (c < 4 * 32 * 8) { const int q = c >> 3; lru_out_loadps(args, q >> 5, 4 + (q & 31), c & 7, __builtin_amdgcn_readfirstlane(tid >> 6) * 64 + fresh_lane(), psw); }
;         for (int u = c; u < 4 * 32 * 8; u += G) { const int blk = u & 7, q = u >> 3; const int un = u + G, qn = un >> 3; const bool hn = un < 4 * 32 * 8;
.LBB0_667:
	s_cmp_eq_u32 s100, 2
	s_cbranch_scc1 .LBB0_684
	v_readlane_b32 s0, v249, 24
	s_cmpk_lt_i32 s83, 0x400
	v_readlane_b32 s1, v249, 25
	s_cbranch_scc0 .LBB0_685
	s_lshl_b32 s0, s83, 7
	s_and_b32 s3, s0, 0x380
	s_waitcnt lgkmcnt(0)
	s_add_u32 s4, s84, 0x4800000
	s_addc_u32 s5, s85, 0
	s_lshl_b32 s6, s83, 3
	s_ashr_i32 s1, s83, 7
	s_and_b32 s6, s6, 0x7c0
	s_and_b32 s2, s1, -2
	s_add_i32 s10, s6, 0x100
	s_or_b32 s1, s1, 1
	s_add_u32 s6, s84, 0x25200000
	s_addc_u32 s7, s85, 0
	s_mul_hi_i32 s13, s1, 0x900
	s_mul_i32 s14, s1, 0x900
	s_add_u32 s1, s84, 0x3d200000
	s_mul_hi_i32 s11, s2, 0x900
	s_mul_i32 s12, s2, 0x900
	s_addc_u32 s2, s85, 0
	s_add_u32 s8, s84, 0x3c200000
	v_readlane_b32 s15, v249, 0
	s_addc_u32 s9, s85, 0
	s_lshr_b32 s15, s15, 6
	v_mbcnt_lo_u32_b32 v0, -1, 0
	v_mbcnt_hi_u32_b32 v0, -1, v0
	s_lshl_b32 s16, s15, 6
	v_or_b32_e32 v0, s3, v0
	s_lshl_b32 s3, s15, 3
	s_and_b32 s3, s3, -16
	s_ashr_i32 s15, s3, 31
	v_and_or_b32 v64, s16, 64, v0
	s_add_u32 s16, s3, s10
	s_addc_u32 s15, s15, 0
	s_add_u32 s10, s16, s12
	v_mov_b32_e32 v65, 0
	s_addc_u32 s11, s15, s11
	v_lshl_add_u64 v[0:1], v[64:65], 2, s[4:5]
	s_lshl_b64 s[10:11], s[10:11], 12
	v_lshl_add_u64 v[2:3], v[0:1], 0, s[10:11]
	s_movk_i32 s3, 0x2000
	v_add_co_u32_e32 v4, vcc, s3, v2
	s_movk_i32 s33, 0x4000
	s_nop 0
	v_addc_co_u32_e32 v5, vcc, 0, v3, vcc
	v_add_co_u32_e32 v6, vcc, s33, v2
	s_movk_i32 s38, 0x6000
	s_nop 0
	v_addc_co_u32_e32 v7, vcc, 0, v3, vcc
	v_add_co_u32_e32 v8, vcc, s38, v2
	s_mov_b32 s39, 0x8000
	s_nop 0
	v_addc_co_u32_e32 v9, vcc, 0, v3, vcc
	v_add_co_u32_e32 v10, vcc, s39, v2
	s_mov_b32 s44, 0xa000
	s_nop 0
	v_addc_co_u32_e32 v11, vcc, 0, v3, vcc
	s_waitcnt vmcnt(0)
	v_add_co_u32_e32 v12, vcc, s44, v2
	s_mov_b32 s45, 0xc000
	s_nop 0
	v_addc_co_u32_e32 v13, vcc, 0, v3, vcc
	v_add_co_u32_e32 v14, vcc, s45, v2
	s_mov_b32 s50, 0xe000
	s_nop 0
	v_addc_co_u32_e32 v15, vcc, 0, v3, vcc
	global_load_dword v37, v[8:9], off offset:-4096
	global_load_dword v38, v[8:9], off
	global_load_dword v39, v[10:11], off offset:-4096
	global_load_dword v40, v[10:11], off
	global_load_dword v41, v[12:13], off offset:-4096
	global_load_dword v42, v[12:13], off
	global_load_dword v43, v[14:15], off offset:-4096
	global_load_dword v44, v[14:15], off
	v_add_co_u32_e32 v8, vcc, s50, v2
	s_add_u32 s10, s16, s14
	s_nop 0
	v_addc_co_u32_e32 v9, vcc, 0, v3, vcc
	s_mov_b32 s51, 0xf000
	s_addc_u32 s11, s15, s13
	v_add_co_u32_e32 v10, vcc, s51, v2
	s_lshl_b64 s[10:11], s[10:11], 12
	s_nop 0
	v_addc_co_u32_e32 v11, vcc, 0, v3, vcc
	v_lshl_add_u64 v[0:1], v[0:1], 0, s[10:11]
	v_add_co_u32_e32 v12, vcc, s3, v0
	s_lshl_b32 s72, s82, 7
	s_nop 0
	v_addc_co_u32_e32 v13, vcc, 0, v1, vcc
	v_add_co_u32_e32 v14, vcc, s33, v0
	s_movk_i32 s73, 0x7fff
	s_nop 0
	v_addc_co_u32_e32 v15, vcc, 0, v1, vcc
	v_add_co_u32_e32 v16, vcc, s38, v0
	s_mov_b32 s74, s83
	s_nop 0
	v_addc_co_u32_e32 v17, vcc, 0, v1, vcc
	global_load_dword v45, v[8:9], off offset:-4096
	global_load_dword v46, v[8:9], off
	global_load_dword v49, v[12:13], off offset:-4096
	global_load_dword v50, v[12:13], off
	global_load_dword v51, v[14:15], off offset:-4096
	global_load_dword v52, v[14:15], off
	global_load_dword v53, v[16:17], off offset:-4096
	global_load_dword v54, v[16:17], off
	v_add_co_u32_e32 v8, vcc, s39, v0
	s_nop 1
	v_addc_co_u32_e32 v9, vcc, 0, v1, vcc
	v_add_co_u32_e32 v12, vcc, s44, v0
	s_nop 1
	v_addc_co_u32_e32 v13, vcc, 0, v1, vcc
	v_add_co_u32_e32 v14, vcc, s45, v0
	s_nop 1
	v_addc_co_u32_e32 v15, vcc, 0, v1, vcc
	v_add_co_u32_e32 v16, vcc, s50, v0
	s_nop 1
	v_addc_co_u32_e32 v17, vcc, 0, v1, vcc
	global_load_dword v55, v[8:9], off offset:-4096
	global_load_dword v56, v[8:9], off
	global_load_dword v57, v[12:13], off offset:-4096
	global_load_dword v58, v[12:13], off
	global_load_dword v59, v[14:15], off offset:-4096
	global_load_dword v60, v[14:15], off
	global_load_dword v61, v[16:17], off offset:-4096
	global_load_dword v62, v[16:17], off
	v_add_co_u32_e32 v8, vcc, s51, v0
	s_nop 1
	v_addc_co_u32_e32 v9, vcc, 0, v1, vcc
	global_load_dword v32, v[2:3], off
	global_load_dword v33, v[4:5], off offset:-4096
	global_load_dword v34, v[4:5], off
	global_load_dword v35, v[6:7], off offset:-4096
	global_load_dword v36, v[6:7], off
	global_load_dword v47, v[10:11], off
	global_load_dword v48, v[0:1], off
	global_load_dword v63, v[8:9], off
	s_waitcnt vmcnt(0)
	v_mov_b64_e32 v[0:1], v[32:33]
	v_mov_b64_e32 v[2:3], v[34:35]
	v_mov_b64_e32 v[4:5], v[36:37]
	v_mov_b64_e32 v[6:7], v[38:39]
	v_mov_b64_e32 v[8:9], v[40:41]
	v_mov_b64_e32 v[10:11], v[42:43]
	v_mov_b64_e32 v[12:13], v[44:45]
	v_mov_b64_e32 v[14:15], v[46:47]
	v_mov_b64_e32 v[16:17], v[48:49]
	v_mov_b64_e32 v[18:19], v[50:51]
	v_mov_b64_e32 v[20:21], v[52:53]
	v_mov_b64_e32 v[22:23], v[54:55]
	v_mov_b64_e32 v[24:25], v[56:57]
	v_mov_b64_e32 v[26:27], v[58:59]
	v_mov_b64_e32 v[28:29], v[60:61]
	v_mov_b64_e32 v[30:31], v[62:63]
	s_branch .LBB0_670

; __device__ __forceinline__ int fresh_lane() { int l; asm volatile("v_mbcnt_lo_u32_b32 %0, -1, 0\n\tv_mbcnt_hi_u32_b32 %0, -1, %0" : "=v"(l)); __builtin_assume(l >= 0 && l < 64); return l; }
; #define FRESH() const int tid = TID(), lane = tid & 63, wave = __builtin_amdgcn_readfirstlane(tid >> 6); (void)lane; (void)wave
; #define PH(k, ...) if (IN(k)) { _Pragma("unroll") for (int rep_ = 0; rep_ < ((DUP_PHASE) == (k) ? 2 : 1); ++rep_) { if (rep_) xcd_barrier(bar, TID()); __VA_ARGS__ } } SEAM(k);
; __global__ void __launch_bounds__(NTHR, 2) fwd_kernel(Args args) {
;     ...
;     PH(3, { FRESH();
;         for (int u = c; u < 256; u += G) ml_out_unit(args, lds, u, tid);
;         unsigned psw[2][16];
;         if (c < 4 * 32 * 8) { const int q = c >> 3; lru_out_loadps(args, q >> 5, 4 + (q & 31), c & 7, __builtin_amdgcn_readfirstlane(tid >> 6) * 64 + fresh_lane(), psw); }
;         for (int u = c; u < 4 * 32 * 8; u += G) { const int blk = u & 7, q = u >> 3; const int un = u + G, qn = un >> 3; const bool hn = un < 4 * 32 * 8;
;             lru_out_unit(args, lds, q >> 5, 4 + (q & 31), blk, tid, psw, hn ? qn >> 5 : 0, hn ? 4 + (qn & 31) : -1, un & 7); } })
.LBB0_684:
	s_cmp_eq_u32 s100, 1
	s_cbranch_scc0 .Lp3_done
	s_mov_b32 s100, 2
	s_load_dwordx2 s[58:59], s[96:97], 0x48
	s_waitcnt lgkmcnt(0)
	s_branch .Lp3_ml

; __device__ __forceinline__ unsigned xb_ld(unsigned* p)              { return __hip_atomic_load(p, __ATOMIC_RELAXED, __HIP_MEMORY_SCOPE_AGENT); }
; __device__ __forceinline__ unsigned xb_add(unsigned* p, unsigned v) { return __hip_atomic_fetch_add(p, v, __ATOMIC_RELAXED, __HIP_MEMORY_SCOPE_AGENT); }
; #define XB_SPIN(cond, bar) do { unsigned _sp = 0; while (cond) { __builtin_amdgcn_s_sleep(1); \
;     if ((++_sp & 255u) == 0u) { if (xb_ld(&(bar)[XB_TMO])) break; if (_sp > XB_SPIN_CAP) { atomicAdd(&(bar)[XB_TMO], 1u); break; } } } } while (0)
; __device__ __forceinline__ void xcd_barrier(const XcdBarrier& b, int tid) {
;     ...
;         const unsigned old = xb_add(&bar[XB_XSUB(b.x)], 1u);
;         const unsigned gen = old / nloc;
;         if (old + 1u == (gen + 1u) * nloc) {
;             __builtin_amdgcn_fence(__ATOMIC_RELEASE, "agent");
;             asm volatile("s_waitcnt vmcnt(0)" ::: "memory");
;             const unsigned og = xb_add(&bar[XB_TOP], 1u);
;             const unsigned tg = og / nx;
;             if (og + 1u == (tg + 1u) * nx) xb_add(&bar[XB_TOPGEN], 1u);
;             else XB_SPIN(xb_ld(&bar[XB_TOPGEN]) == tg, bar);
;             __builtin_amdgcn_fence(__ATOMIC_ACQUIRE, "agent");
;             xb_add(&bar[XB_XGEN(b.x)], 1u);
;             asm volatile("s_waitcnt vmcnt(0)" ::: "memory");
;         } else {
;             XB_SPIN(xb_ld(&bar[XB_XGEN(b.x)]) == gen, bar);
;             __builtin_amdgcn_fence(__ATOMIC_ACQUIRE, "agent");
;             asm volatile("s_waitcnt vmcnt(0)" ::: "memory");
;         }
.LBB0_1130:
	v_readlane_b32 s2, v249, 2
	s_lshl_b32 s2, s2, 8
	v_readlane_b32 s6, v249, 3
	v_readlane_b32 s7, v249, 4
	s_add_u32 s6, s6, s2
	s_addc_u32 s7, s7, 0
	v_mov_b32_e32 v1, 0x1000
	v_mov_b32_e32 v3, 1
	v_sub_u32_e32 v4, 0, v2
	global_atomic_add v3, v1, v3, s[6:7] offset:1024 sc0
	v_cvt_f32_u32_e32 v1, v2
	v_rcp_iflag_f32_e32 v1, v1
	s_nop 0
	v_mul_f32_e32 v1, 0x4f7ffffe, v1
	v_cvt_u32_f32_e32 v1, v1
	v_mul_lo_u32 v4, v4, v1
	v_mul_hi_u32 v4, v1, v4
	v_add_u32_e32 v1, v1, v4
	s_waitcnt vmcnt(0)
	v_mul_hi_u32 v1, v3, v1
	v_mul_lo_u32 v4, v1, v2
	v_sub_u32_e32 v4, v3, v4
	v_add_u32_e32 v5, 1, v1
	v_cmp_ge_u32_e32 vcc, v4, v2
	v_add_u32_e32 v3, 1, v3
	s_nop 0
	v_cndmask_b32_e32 v1, v1, v5, vcc
	v_sub_u32_e32 v5, v4, v2
	v_cndmask_b32_e32 v4, v4, v5, vcc
	v_add_u32_e32 v5, 1, v1
	v_cmp_ge_u32_e32 vcc, v4, v2
	s_nop 1
	v_cndmask_b32_e32 v1, v1, v5, vcc
	v_mul_lo_u32 v4, v2, v1
	v_add_u32_e32 v2, v4, v2
	v_cmp_ne_u32_e32 vcc, v3, v2
	s_and_saveexec_b64 s[2:3], vcc
	s_xor_b64 s[16:17], exec, s[2:3]
	s_cbranch_execz .LBB0_1144
	s_waitcnt lgkmcnt(0)
	buffer_inv sc1
	v_mov_b32_e32 v0, 0x7100
	global_load_dword v0, v0, s[84:85] offset:1024 sc1
	s_add_u32 s22, s84, 0x7500
	s_addc_u32 s23, s85, 0
	s_waitcnt vmcnt(0)
	v_cmp_eq_u32_e32 vcc, v0, v1
	s_and_saveexec_b64 s[18:19], vcc
	s_cbranch_execz .LBB0_1143
	s_add_u32 s20, s84, 0x4200
	s_addc_u32 s21, s85, 0
	s_mov_b32 s2, 1
	s_mov_b64 s[24:25], 0
	v_mov_b32_e32 v0, 0
	s_branch .LBB0_1134

; template <int MODE>
; __device__ __forceinline__ int moe_gemm(const Args& a, unsigned char* lds_g, int tid, int idx0) {
;     ...
;         const int bk = w, bp = lane;
;         int e = 0;
; #pragma unroll 1
;         for (int q = 1; q < NEXP; ++q) e = (cum[q] <= ti) ? q : e;
;         e = __builtin_amdgcn_readfirstlane(e);
;         const int mt = __builtin_amdgcn_readfirstlane(ti - cum[e]);
;         unsigned aofs[4]; unsigned bofs; int bwr0;
;         __amdgpu_buffer_rsrc_t rsA, rsB, rsB3;
;         if (MODE == 1) { const int cnt = cum[128 + e];
; #pragma unroll
;             for (int q = 0; q < 2; ++q) { const int pos = 256 * mt + 128 * q + (tidu >> 2); const int tok = pos < cnt ? ((const int*)(a.ws + WS_LIST))[e * 8192 + pos] : 0;
;                 aofs[q] = (unsigned)(tok * D + 16 * (tidu & 3)); }
.LBB0_1175:
	v_mov_b32_e32 v1, s7
	ds_read_b32 v1, v1
	v_mov_b32_e32 v3, s6
	s_add_i32 s6, s6, 1
	s_add_i32 s7, s7, 4
	s_cmp_eq_u32 s6, 32
	s_waitcnt lgkmcnt(0)
	v_cmp_lt_i32_e32 vcc, s38, v1
	s_nop 1
	v_cndmask_b32_e32 v0, v3, v0, vcc
	s_cbranch_scc0 .LBB0_1175
	v_readfirstlane_b32 s6, v0
	s_lshl_b32 s7, s6, 2
	s_add_i32 s7, s7, 0
	s_add_i32 s7, s7, 0x22800
	v_mov_b32_e32 v0, s7
	ds_read2st64_b32 v[0:1], v0 offset1:2
	v_or_b32_e32 v4, s45, v2
	v_ashrrev_i32_e32 v4, 2, v4
	v_mov_b32_e32 v3, 0
	s_lshl_b32 s7, s6, 13
	s_waitcnt lgkmcnt(0)
	v_sub_u32_e32 v0, s38, v0
	s_nop 0
	v_readfirstlane_b32 s16, v0
	v_readfirstlane_b32 s8, v1
	s_lshl_b32 s9, s16, 8
	s_sub_i32 s8, s8, s9
	v_writelane_b32 v249, s8, 50
	v_mov_b32_e32 v0, 0
	s_nop 0
	v_lshl_add_u32 v4, s16, 8, v4
	v_cmp_lt_i32_e32 vcc, v4, v1
	s_and_saveexec_b64 s[16:17], vcc
	s_cbranch_execz .LBB0_1178
	v_add_u32_e32 v6, s7, v4
	v_ashrrev_i32_e32 v7, 31, v6
	v_lshl_add_u64 v[6:7], v[6:7], 2, s[28:29]
	global_load_dword v0, v[6:7], off
	s_waitcnt vmcnt(0)
	v_lshlrev_b32_e32 v0, 11, v0

; #define MG_BAR() do { asm volatile("s_waitcnt lgkmcnt(0)" ::: "memory"); __builtin_amdgcn_s_barrier(); asm volatile("" ::: "memory"); } while (0)
; #define MH_LDA(te_, to_) do { ra[0] = __builtin_amdgcn_raw_buffer_load_b128(rsA, aofs[0], 64 * (te_), 0); ra[1] = __builtin_amdgcn_raw_buffer_load_b128(rsA, aofs[1], 64 * (te_), 0); \
;             ra[2] = __builtin_amdgcn_raw_buffer_load_b128(rsA, aofs[0], 64 * (to_), 0); ra[3] = __builtin_amdgcn_raw_buffer_load_b128(rsA, aofs[1], 64 * (to_), 0); } while (0)
; template <int MODE>
; __device__ __forceinline__ int moe_gemm(const Args& a, unsigned char* lds_g, int tid, int idx0) {
;     ...
;         if (MODE == 1) { const int cnt = cum[128 + e];
; #pragma unroll
;             for (int q = 0; q < 2; ++q) { const int pos = 256 * mt + 128 * q + (tidu >> 2); const int tok = pos < cnt ? ((const int*)(a.ws + WS_LIST))[e * 8192 + pos] : 0;
;                 aofs[q] = (unsigned)(tok * D + 16 * (tidu & 3)); }
;             aofs[2] = aofs[3] = 0u;
;             rsA = __builtin_amdgcn_make_buffer_rsrc((void*)(a.ws + WS_H2), 0, 0x7fffffff, 0x00020000);
;             rsB = __builtin_amdgcn_make_buffer_rsrc((void*)(a.in[I_W1] + (size_t)e * D * DE), 0, 0x7fffffff, 0x00020000); rsB3 = __builtin_amdgcn_make_buffer_rsrc((void*)(a.in[I_W3] + (size_t)e * D * DE), 0, 0x7fffffff, 0x00020000);
;             bofs = (unsigned)((bk + 8 * (bp >> 5)) * DE + 128 * nt + 4 * (bp & 31)) * 4u;
;             bwr0 = MH_BROW * (2 * (bk & 3) + (bk >> 2) + 8 * (bp >> 5)) + 2 * (128 * ((bp & 31) >> 4) + 16 * (bp & 3) + 4 * ((bp & 15) >> 2)); }
;     ...
;             MH_LDA(0, 1); MH_LDB(0);
;             MG_BAR();
.LBB0_1180:
	s_or_b64 exec, exec, s[16:17]
	s_ashr_i32 s7, s6, 31
	v_readlane_b32 s8, v249, 6
	v_lshlrev_b32_e32 v1, 4, v2
	s_lshl_b64 s[6:7], s[6:7], 23
	v_readlane_b32 s22, v249, 20
	v_and_b32_e32 v52, 48, v1
	v_readlane_b32 s17, v249, 15
	v_readlane_b32 s23, v249, 21
	s_add_u32 s76, s22, s6
	v_or_b32_e32 v191, v3, v52
	v_readlane_b32 s20, v249, 18
	s_addc_u32 s17, s23, s7
	v_lshrrev_b32_e32 v3, 5, v2
	v_or_b32_e32 v188, v0, v52
	v_lshlrev_b32_e32 v0, 2, v2
	s_add_u32 s20, s88, s6
	v_lshlrev_b32_e32 v53, 3, v3
	v_readlane_b32 s21, v249, 19
	s_addc_u32 s6, s89, s7
	v_add_lshl_u32 v4, v53, s44, 10
	v_and_b32_e32 v5, 0x7c, v0
	v_or3_b32 v4, v4, v5, s43
	s_and_b32 s21, s6, 0xffff
	s_mov_b32 s6, s78
	s_mov_b32 s7, s79
	s_and_b32 s77, s17, 0xffff
	s_mov_b32 s22, s78
	s_mov_b32 s23, s79
	v_lshlrev_b32_e32 v192, 2, v4
	buffer_load_dwordx4 v[4:7], v188, s[4:7], 0 offen
	buffer_load_dwordx4 v[20:23], v188, s[4:7], 64 offen
	buffer_load_dwordx4 v[12:15], v191, s[4:7], 0 offen
	buffer_load_dwordx4 v[8:11], v191, s[4:7], 64 offen
	buffer_load_dwordx4 v[16:19], v192, s[76:79], 0 offen
	buffer_load_dwordx4 v[24:27], v192, s[76:79], s48 offen
	buffer_load_dwordx4 v[28:31], v192, s[20:23], 0 offen
	buffer_load_dwordx4 v[32:35], v192, s[20:23], s48 offen
	buffer_load_dwordx4 v[36:39], v192, s[76:79], s79 offen
	buffer_load_dwordx4 v[40:43], v192, s[76:79], s59 offen
	buffer_load_dwordx4 v[44:47], v192, s[20:23], s79 offen
	buffer_load_dwordx4 v[48:51], v192, s[20:23], s59 offen
	v_lshlrev_b32_e32 v54, 6, v2
	v_and_b32_e32 v55, 48, v2
	v_lshrrev_b32_e32 v56, 1, v2
	v_lshlrev_b32_e32 v57, 3, v2
	v_and_b32_e32 v58, 12, v2
	v_lshlrev_b32_e32 v59, 5, v2
	v_and_b32_e32 v60, 32, v0
	v_and_or_b32 v54, v54, s57, v55
	v_and_b32_e32 v0, 0x80, v57
	v_and_b32_e32 v55, 14, v56
	v_and_b32_e32 v1, 0x3c0, v1
	v_and_or_b32 v56, v56, 1, s50
	v_and_b32_e32 v2, 32, v2
	v_add_u32_e32 v53, s47, v53
	v_or3_b32 v0, v58, v0, v52
	v_and_or_b32 v1, v59, 32, v1
	v_lshlrev_b32_e32 v52, 10, v56
	v_lshl_or_b32 v3, v3, 4, v55
	v_mul_lo_u32 v53, v53, s58
	v_bitop3_b32 v1, v1, v52, v2 bitop3:0xde
	v_mul_u32_u24_e32 v56, 0x210, v3
	v_lshl_add_u32 v58, v0, 1, v53
	v_add_u32_e32 v193, 0, v1
	s_waitcnt lgkmcnt(0)
	s_barrier
; #define MG_BAR() do { asm volatile("s_waitcnt lgkmcnt(0)" ::: "memory"); __builtin_amdgcn_s_barrier(); asm volatile("" ::: "memory"); } while (0)
; #define MH_LDA(te_, to_) do { ra[0] = __builtin_amdgcn_raw_buffer_load_b128(rsA, aofs[0], 64 * (te_), 0); ra[1] = __builtin_amdgcn_raw_buffer_load_b128(rsA, aofs[1], 64 * (te_), 0); \
;             ra[2] = __builtin_amdgcn_raw_buffer_load_b128(rsA, aofs[0], 64 * (to_), 0); ra[3] = __builtin_amdgcn_raw_buffer_load_b128(rsA, aofs[1], 64 * (to_), 0); } while (0)
; #define MH_STB(buf_) do { _Pragma("unroll") for (int j_ = 0; j_ < 8; ++j_) { pg8::u32x2 o_; o_.x = pk2(rb[j_].x, rb[j_].y); o_.y = pk2(rb[j_].z, rb[j_].w); \
;             *(pg8::u32x2*)(lds_g + MH_B + (buf_) * MH_BBYTES + bwr0 + (MODE == 1 ? (j_ >> 1) * 16 * MH_BROW + (j_ & 1) * 128 : j_ * 8 * MH_BROW)) = o_; } } while (0)
; template <int MODE>
; __device__ __forceinline__ int moe_gemm(const Args& a, unsigned char* lds_g, int tid, int idx0) {
;     ...
;         f32x4 acc[4][8];
; #pragma unroll
;         for (int m = 0; m < 4; ++m)
; #pragma unroll
;             for (int n = 0; n < 8; ++n) acc[m][n] = (f32x4){0.f, 0.f, 0.f, 0.f};
;     ...
;             MH_LDA(0, 1); MH_LDB(0);
;             MG_BAR();
;             MH_STA(0, 0); MH_STB(0);
;             MH_LDB(1);
	v_and_b32_e32 v61, 16, v57
	s_movk_i32 s26, 0x80
	s_mov_b32 s65, 0
	v_and_b32_e32 v57, 8, v57
	v_add_u32_e32 v55, s49, v61
	v_readlane_b32 s9, v249, 7
	v_readlane_b32 s10, v249, 8
	v_readlane_b32 s11, v249, 9
	v_readlane_b32 s12, v249, 10
	v_readlane_b32 s13, v249, 11
	v_readlane_b32 s14, v249, 12
	v_readlane_b32 s15, v249, 13
	v_readlane_b32 s16, v249, 14
	v_readlane_b32 s18, v249, 16
	v_readlane_b32 s19, v249, 17
	s_waitcnt vmcnt(11)
	v_cvt_pk_f32_fp8_e32 v[0:1], v4
	v_cvt_pk_f32_fp8_sdwa v[2:3], v4 src0_sel:WORD_1
	v_cvt_pk_f32_fp8_e32 v[52:53], v5
	v_cvt_pk_f32_fp8_sdwa v[4:5], v5 src0_sel:WORD_1
	v_cvt_pk_bf16_f32 v0, v0, v1
	v_cvt_pk_bf16_f32 v1, v2, v3
	v_cvt_pk_bf16_f32 v2, v52, v53
	v_cvt_pk_bf16_f32 v3, v4, v5
	ds_write_b128 v193, v[0:3]
	v_cvt_pk_f32_fp8_e32 v[0:1], v6
	v_cvt_pk_f32_fp8_sdwa v[2:3], v6 src0_sel:WORD_1
	v_cvt_pk_f32_fp8_e32 v[4:5], v7
	v_cvt_pk_f32_fp8_sdwa v[6:7], v7 src0_sel:WORD_1
	v_cvt_pk_bf16_f32 v0, v0, v1
	v_cvt_pk_bf16_f32 v1, v2, v3
	v_cvt_pk_bf16_f32 v2, v4, v5
	v_cvt_pk_bf16_f32 v3, v6, v7
	ds_write_b128 v193, v[0:3] offset:16
	s_waitcnt vmcnt(9)
	v_cvt_pk_f32_fp8_e32 v[0:1], v12
	v_cvt_pk_f32_fp8_sdwa v[2:3], v12 src0_sel:WORD_1
	v_cvt_pk_f32_fp8_e32 v[4:5], v13
	v_cvt_pk_f32_fp8_sdwa v[6:7], v13 src0_sel:WORD_1
	v_cvt_pk_bf16_f32 v0, v0, v1
	v_cvt_pk_bf16_f32 v1, v2, v3
	v_cvt_pk_bf16_f32 v2, v4, v5
	v_cvt_pk_bf16_f32 v3, v6, v7
	ds_write_b128 v193, v[0:3] offset:16384
	v_cvt_pk_f32_fp8_e32 v[0:1], v14
	v_cvt_pk_f32_fp8_sdwa v[2:3], v14 src0_sel:WORD_1
	v_cvt_pk_f32_fp8_e32 v[4:5], v15
	v_cvt_pk_f32_fp8_sdwa v[6:7], v15 src0_sel:WORD_1
	v_cvt_pk_bf16_f32 v0, v0, v1
	v_cvt_pk_bf16_f32 v1, v2, v3
	v_cvt_pk_bf16_f32 v2, v4, v5
	v_cvt_pk_bf16_f32 v3, v6, v7
	ds_write_b128 v193, v[0:3] offset:16400
	v_add_u32_e32 v194, 0, v58
	v_add_u32_e32 v195, 0x10000, v194
	s_waitcnt vmcnt(7)
	v_cvt_pk_bf16_f32 v0, v16, v17
	v_cvt_pk_bf16_f32 v1, v18, v19
	s_waitcnt vmcnt(5)
	v_cvt_pk_bf16_f32 v2, v28, v29
	v_cvt_pk_bf16_f32 v3, v30, v31
	ds_write2_b64 v195, v[0:1], v[2:3] offset1:16
	v_cvt_pk_bf16_f32 v0, v24, v25
	v_cvt_pk_bf16_f32 v1, v26, v27
	s_waitcnt vmcnt(4)
	v_cvt_pk_bf16_f32 v2, v32, v33
	v_cvt_pk_bf16_f32 v3, v34, v35
	v_add_u32_e32 v5, 0x2000, v195
	ds_write2_b64 v5, v[0:1], v[2:3] offset0:32 offset1:48
	s_waitcnt vmcnt(3)
	v_cvt_pk_bf16_f32 v0, v36, v37
	v_cvt_pk_bf16_f32 v1, v38, v39
	s_waitcnt vmcnt(1)
	v_cvt_pk_bf16_f32 v2, v44, v45
	v_cvt_pk_bf16_f32 v3, v46, v47
	v_add_u32_e32 v5, 0x4000, v195
	ds_write2_b64 v5, v[0:1], v[2:3] offset0:64 offset1:80
	v_cvt_pk_bf16_f32 v0, v40, v41
	v_cvt_pk_bf16_f32 v1, v42, v43
	s_waitcnt vmcnt(0)
	v_cvt_pk_bf16_f32 v2, v48, v49
	v_cvt_pk_bf16_f32 v3, v50, v51
	v_add_u32_e32 v5, 0x6000, v195
	ds_write2_b64 v5, v[0:1], v[2:3] offset0:96 offset1:112
	buffer_load_dwordx4 v[124:127], v192, s[76:79], s60 offen
	buffer_load_dwordx4 v[92:95], v192, s[76:79], s61 offen
	buffer_load_dwordx4 v[120:123], v192, s[20:23], s60 offen
	buffer_load_dwordx4 v[100:103], v192, s[20:23], s61 offen
	buffer_load_dwordx4 v[104:107], v192, s[76:79], s62 offen
	buffer_load_dwordx4 v[108:111], v192, s[76:79], s63 offen
	buffer_load_dwordx4 v[112:115], v192, s[20:23], s62 offen
	buffer_load_dwordx4 v[116:119], v192, s[20:23], s63 offen
	v_bitop3_b32 v4, v54, s46, v60 bitop3:0xde
	v_mov_b32_e32 v0, 0
	v_add3_u32 v196, v55, v56, v57
	v_add_u32_e32 v197, s51, v4
	v_mov_b32_e32 v1, v0
	v_mov_b32_e32 v2, v0
	v_mov_b32_e32 v3, v0
	v_mov_b32_e32 v4, v0
	v_mov_b32_e32 v5, v0
	v_mov_b32_e32 v6, v0
	v_mov_b32_e32 v7, v0
	v_mov_b32_e32 v24, v0
	v_mov_b32_e32 v25, v0
	v_mov_b32_e32 v26, v0
	v_mov_b32_e32 v27, v0
	v_mov_b32_e32 v28, v0
	v_mov_b32_e32 v29, v0
	v_mov_b32_e32 v30, v0
	v_mov_b32_e32 v31, v0
	v_mov_b32_e32 v12, v0
	v_mov_b32_e32 v13, v0
	v_mov_b32_e32 v14, v0
	v_mov_b32_e32 v15, v0
	v_mov_b32_e32 v16, v0
	v_mov_b32_e32 v17, v0
	v_mov_b32_e32 v18, v0
	v_mov_b32_e32 v19, v0
	v_mov_b32_e32 v32, v0
	v_mov_b32_e32 v33, v0
	v_mov_b32_e32 v34, v0
	v_mov_b32_e32 v35, v0
	v_mov_b32_e32 v36, v0
	v_mov_b32_e32 v37, v0
	v_mov_b32_e32 v38, v0
	v_mov_b32_e32 v39, v0
	v_mov_b32_e32 v40, v0
	v_mov_b32_e32 v41, v0
	v_mov_b32_e32 v42, v0
	v_mov_b32_e32 v43, v0
	v_mov_b32_e32 v44, v0
	v_mov_b32_e32 v45, v0
	v_mov_b32_e32 v46, v0
	v_mov_b32_e32 v47, v0
	v_mov_b32_e32 v56, v0
	v_mov_b32_e32 v57, v0
	v_mov_b32_e32 v58, v0
	v_mov_b32_e32 v59, v0
	v_mov_b32_e32 v60, v0
	v_mov_b32_e32 v61, v0
	v_mov_b32_e32 v62, v0
	v_mov_b32_e32 v63, v0
	v_mov_b32_e32 v48, v0
	v_mov_b32_e32 v49, v0
	v_mov_b32_e32 v50, v0
	v_mov_b32_e32 v51, v0
	v_mov_b32_e32 v52, v0
	v_mov_b32_e32 v53, v0
	v_mov_b32_e32 v54, v0
	v_mov_b32_e32 v55, v0
	v_mov_b32_e32 v64, v0
	v_mov_b32_e32 v65, v0
	v_mov_b32_e32 v66, v0
	v_mov_b32_e32 v67, v0
	v_mov_b32_e32 v68, v0
	v_mov_b32_e32 v69, v0
	v_mov_b32_e32 v70, v0
	v_mov_b32_e32 v71, v0
	v_mov_b32_e32 v72, v0
	v_mov_b32_e32 v73, v0
	v_mov_b32_e32 v74, v0
	v_mov_b32_e32 v75, v0
	v_mov_b32_e32 v76, v0
	v_mov_b32_e32 v77, v0
	v_mov_b32_e32 v78, v0
	v_mov_b32_e32 v79, v0
	v_mov_b32_e32 v88, v0
	v_mov_b32_e32 v89, v0
	v_mov_b32_e32 v90, v0
	v_mov_b32_e32 v91, v0
	v_mov_b32_e32 v96, v0
	v_mov_b32_e32 v97, v0
	v_mov_b32_e32 v98, v0
	v_mov_b32_e32 v99, v0
	v_mov_b32_e32 v80, v0
	v_mov_b32_e32 v81, v0
	v_mov_b32_e32 v82, v0
	v_mov_b32_e32 v83, v0
	v_mov_b32_e32 v84, v0
	v_mov_b32_e32 v85, v0
	v_mov_b32_e32 v86, v0
	v_mov_b32_e32 v87, v0
	v_mov_b32_e32 v128, v0
	v_mov_b32_e32 v129, v0
	v_mov_b32_e32 v130, v0
	v_mov_b32_e32 v131, v0
	v_mov_b32_e32 v140, v0
	v_mov_b32_e32 v141, v0
	v_mov_b32_e32 v142, v0
	v_mov_b32_e32 v143, v0
	v_mov_b32_e32 v132, v0
	v_mov_b32_e32 v133, v0
	v_mov_b32_e32 v134, v0
	v_mov_b32_e32 v135, v0
	v_mov_b32_e32 v136, v0
	v_mov_b32_e32 v137, v0
	v_mov_b32_e32 v138, v0
	v_mov_b32_e32 v139, v0
	v_mov_b32_e32 v152, v0
	v_mov_b32_e32 v153, v0
	v_mov_b32_e32 v154, v0
	v_mov_b32_e32 v155, v0
	v_mov_b32_e32 v156, v0
	v_mov_b32_e32 v157, v0
	v_mov_b32_e32 v158, v0
	v_mov_b32_e32 v159, v0
	v_mov_b32_e32 v144, v0
	v_mov_b32_e32 v145, v0
	v_mov_b32_e32 v146, v0
	v_mov_b32_e32 v147, v0
	v_mov_b32_e32 v148, v0
	v_mov_b32_e32 v149, v0
	v_mov_b32_e32 v150, v0
	v_mov_b32_e32 v151, v0
	v_mov_b32_e32 v160, v0
	v_mov_b32_e32 v161, v0
	v_mov_b32_e32 v162, v0
	v_mov_b32_e32 v163, v0
	v_mov_b32_e32 v164, v0
	v_mov_b32_e32 v165, v0
	v_mov_b32_e32 v166, v0
	v_mov_b32_e32 v167, v0
	v_readlane_b32 s8, v249, 50
	s_lshr_b32 s9, s44, 1
	s_lshl_b32 s9, s9, 6
	s_cmp_ge_i32 s9, s8
	s_cbranch_scc1 .Lnm1_head

; __device__ __forceinline__ float sigmoidf_(float x) { return __builtin_amdgcn_rcpf(1.f + __expf(-x)); }
; __device__ __forceinline__ int fresh_lane() { int l; asm volatile("v_mbcnt_lo_u32_b32 %0, -1, 0\n\tv_mbcnt_hi_u32_b32 %0, -1, %0" : "=v"(l)); __builtin_assume(l >= 0 && l < 64); return l; }
; template <int MODE>
; __device__ __forceinline__ int moe_gemm(const Args& a, unsigned char* lds_g, int tid, int idx0) {
;     ...
;         const int ln_ = fresh_lane();
;         const int efr = ln_ & 15, efq = ln_ >> 4;
;         if (MODE == 1) { unsigned char* HM = (unsigned char*)(a.ws + WS_HM) + (size_t)256 * ti * DE + 128 * nt + 64 * wn; const unsigned lo_ = (unsigned)((128 * hh + 64 * wr + efr) * DE + 16 * efq);
; #pragma unroll
;             for (int m = 0; m < 4; ++m) { v4u o16;
; #pragma unroll
;                 for (int n = 0; n < 4; n += 2) { float hv[8];
; #pragma unroll
;                     for (int r = 0; r < 4; ++r) { const float a1 = acc[m][n][r], a2 = acc[m][n + 1][r]; hv[r] = a1 * sigmoidf_(a1) * acc[m][n + 4][r]; hv[4 + r] = a2 * sigmoidf_(a2) * acc[m][n + 5][r]; }
;                     int w8a = __builtin_amdgcn_cvt_pk_fp8_f32(hv[0], hv[1], 0, false); w8a = __builtin_amdgcn_cvt_pk_fp8_f32(hv[2], hv[3], w8a, true);
;                     int w8b = __builtin_amdgcn_cvt_pk_fp8_f32(hv[4], hv[5], 0, false); w8b = __builtin_amdgcn_cvt_pk_fp8_f32(hv[6], hv[7], w8b, true);
;                     if (n == 0) { o16.x = (unsigned)w8a; o16.y = (unsigned)w8b; } else { o16.z = (unsigned)w8a; o16.w = (unsigned)w8b; } }
;                 { void* p_ = (void*)(HM + lo_ + 16 * m * DE); asm volatile("global_store_dwordx4 %0, %1, off sc1\n\ts_nop 1" :: "v"(p_), "v"(o16) : "memory"); } }
.Lnm1_exit:
	v_mul_f32_e32 v10, 0xbfb8aa3b, v164
	v_exp_f32_e32 v10, v10
	v_mul_f32_e32 v11, 0xbfb8aa3b, v160
	v_exp_f32_e32 v11, v11
	v_mbcnt_lo_u32_b32 v22, -1, 0
	v_mbcnt_hi_u32_b32 v22, -1, v22
	s_mov_b32 s39, s27
	v_and_b32_e32 v8, 48, v22
	v_and_or_b32 v9, v22, 15, s54
	v_lshl_or_b32 v188, v9, 10, v8
	v_add_f32_e32 v8, 1.0, v10
	v_rcp_f32_e32 v8, v8
	v_add_f32_e32 v9, 1.0, v11
	v_rcp_f32_e32 v9, v9
	v_mul_f32_e32 v11, 0xbfb8aa3b, v161
	v_mul_f32_e32 v8, v164, v8
	v_mul_f32_e32 v10, v8, v156
	v_mul_f32_e32 v8, v160, v9
	v_mul_f32_e32 v9, 0xbfb8aa3b, v165
	v_exp_f32_e32 v9, v9
	v_exp_f32_e32 v11, v11
	v_mul_f32_e32 v23, v8, v152
	s_lshl_b64 s[6:7], s[38:39], 18
	v_add_f32_e32 v8, 1.0, v9
	v_rcp_f32_e32 v8, v8
	v_add_f32_e32 v9, 1.0, v11
	v_mul_f32_e32 v11, 0xbfb8aa3b, v166
	v_rcp_f32_e32 v9, v9
	v_exp_f32_e32 v11, v11
	v_mul_f32_e32 v8, v165, v8
	s_waitcnt vmcnt(5)
	v_mul_f32_e32 v92, v8, v157
	v_mul_f32_e32 v8, v161, v9
	v_add_f32_e32 v9, 1.0, v11
	v_rcp_f32_e32 v9, v9
	v_mul_f32_e32 v11, 0xbfb8aa3b, v162
	v_exp_f32_e32 v11, v11
	v_mul_f32_e32 v93, v8, v153
	v_mul_f32_e32 v8, v166, v9
	v_mul_f32_e32 v9, 0xbfb8aa3b, v167
	v_exp_f32_e32 v9, v9
	v_mul_f32_e32 v94, v8, v158
	v_add_f32_e32 v8, 1.0, v11
	v_mul_f32_e32 v11, 0xbfb8aa3b, v163
	v_rcp_f32_e32 v8, v8
	v_exp_f32_e32 v11, v11
	v_add_f32_e32 v9, 1.0, v9
	v_rcp_f32_e32 v9, v9
	v_mul_f32_e32 v8, v162, v8
	v_add_f32_e32 v11, 1.0, v11
	v_rcp_f32_e32 v11, v11
	v_mul_f32_e32 v95, v8, v154
	v_mul_f32_e32 v8, v167, v9
	v_mul_f32_e32 v9, 0xbfb8aa3b, v148
	s_waitcnt vmcnt(4)
	v_exp_f32_e32 v101, v9
	v_mov_b32_e32 v9, v189
	v_cvt_pk_fp8_f32 v9, v23, v93
	v_mul_f32_e32 v23, 0xbfb8aa3b, v144
	v_exp_f32_e32 v23, v23
	v_mul_f32_e32 v100, v8, v159
	v_mul_f32_e32 v8, v163, v11
	v_mul_f32_e32 v11, v8, v155
	v_mov_b32_e32 v8, v189
	v_cvt_pk_fp8_f32 v8, v10, v92
	v_add_f32_e32 v10, 1.0, v101
	v_rcp_f32_e32 v10, v10
	v_cvt_pk_fp8_f32 v9, v95, v11 op_sel:[0,0,1]
	v_add_f32_e32 v11, 1.0, v23
	v_rcp_f32_e32 v11, v11
	v_mul_f32_e32 v23, 0xbfb8aa3b, v149
	v_exp_f32_e32 v23, v23
	v_mul_f32_e32 v10, v148, v10
	v_mul_f32_e32 v92, v10, v136
	v_mul_f32_e32 v10, v144, v11
	v_mul_f32_e32 v11, 0xbfb8aa3b, v145
	v_mul_f32_e32 v93, v10, v132
	v_add_f32_e32 v10, 1.0, v23
	v_exp_f32_e32 v11, v11
	v_mul_f32_e32 v23, 0xbfb8aa3b, v150
	v_exp_f32_e32 v23, v23
	v_rcp_f32_e32 v10, v10
	v_add_f32_e32 v11, 1.0, v11
	v_rcp_f32_e32 v11, v11
	v_add_f32_e32 v23, 1.0, v23
	v_rcp_f32_e32 v23, v23
	v_mul_f32_e32 v10, v149, v10
	v_cvt_pk_fp8_f32 v8, v94, v100 op_sel:[0,0,1]
	v_mul_f32_e32 v94, v10, v137
	v_mul_f32_e32 v10, v145, v11
	v_mul_f32_e32 v11, 0xbfb8aa3b, v146
	v_mul_f32_e32 v95, v10, v133
	v_mul_f32_e32 v10, v150, v23
	v_exp_f32_e32 v11, v11
	v_mul_f32_e32 v23, 0xbfb8aa3b, v151
	v_exp_f32_e32 v23, v23
	v_mul_f32_e32 v100, v10, v138
	v_add_f32_e32 v10, 1.0, v11
	v_rcp_f32_e32 v10, v10
	v_add_f32_e32 v11, 1.0, v23
	v_mul_f32_e32 v23, 0xbfb8aa3b, v147
	v_exp_f32_e32 v23, v23
	v_mul_f32_e32 v10, v146, v10
	v_rcp_f32_e32 v11, v11
	v_mul_f32_e32 v101, v10, v134
	v_add_f32_e32 v10, 1.0, v23
	v_rcp_f32_e32 v23, v10
	v_mov_b32_e32 v10, v189
	v_cvt_pk_fp8_f32 v10, v92, v94
	v_mul_f32_e32 v11, v151, v11
	v_mul_f32_e32 v11, v11, v139
	v_mul_f32_e32 v92, 0xbfb8aa3b, v140
	v_cvt_pk_fp8_f32 v10, v100, v11 op_sel:[0,0,1]
	v_mov_b32_e32 v11, v189
	v_cvt_pk_fp8_f32 v11, v93, v95
	v_exp_f32_e32 v92, v92
	v_mul_f32_e32 v93, 0xbfb8aa3b, v128
	v_exp_f32_e32 v93, v93
	v_mul_f32_e32 v23, v147, v23
	v_mul_f32_e32 v23, v23, v135
	s_add_u32 s6, s52, s6
	v_cvt_pk_fp8_f32 v11, v101, v23 op_sel:[0,0,1]
	v_add_f32_e32 v23, 1.0, v92
	s_addc_u32 s7, s53, s7
	v_rcp_f32_e32 v23, v23
	v_add_f32_e32 v92, 1.0, v93
	v_lshl_add_u64 v[20:21], s[6:7], 0, v[188:189]
	v_rcp_f32_e32 v92, v92
	global_store_dwordx4 v[20:21], v[8:11], off sc1
	s_nop 1
	v_mul_f32_e32 v10, 0xbfb8aa3b, v141
	v_exp_f32_e32 v10, v10
	v_mul_f32_e32 v11, 0xbfb8aa3b, v129
	v_exp_f32_e32 v11, v11
	v_mul_f32_e32 v8, v140, v23
	v_mul_f32_e32 v9, v8, v96
	v_mul_f32_e32 v8, v128, v92
	v_mul_f32_e32 v23, v8, v88
	v_add_f32_e32 v8, 1.0, v10
	v_rcp_f32_e32 v8, v8
	v_add_f32_e32 v10, 1.0, v11
	v_mul_f32_e32 v11, 0xbfb8aa3b, v142
	v_rcp_f32_e32 v10, v10
	v_exp_f32_e32 v11, v11
	v_mul_f32_e32 v8, v141, v8
	v_mul_f32_e32 v88, v8, v97
	v_mul_f32_e32 v8, v129, v10
	v_add_f32_e32 v10, 1.0, v11
	v_rcp_f32_e32 v10, v10
	v_mul_f32_e32 v11, 0xbfb8aa3b, v130
	v_exp_f32_e32 v11, v11
	v_mul_f32_e32 v89, v8, v89
	v_mul_f32_e32 v8, v142, v10
	v_mul_f32_e32 v10, v8, v98
	v_add_f32_e32 v8, 1.0, v11
	v_mul_f32_e32 v11, 0xbfb8aa3b, v143
	v_exp_f32_e32 v11, v11
	v_mul_f32_e32 v92, 0xbfb8aa3b, v131
	v_exp_f32_e32 v92, v92
	v_rcp_f32_e32 v8, v8
	v_add_f32_e32 v11, 1.0, v11
	v_rcp_f32_e32 v11, v11
	v_add_f32_e32 v92, 1.0, v92
	v_rcp_f32_e32 v92, v92
	v_mul_f32_e32 v8, v130, v8
	v_mul_f32_e32 v90, v8, v90
	v_mul_f32_e32 v8, v143, v11
	v_mul_f32_e32 v11, v8, v99
	v_mov_b32_e32 v8, v189
	v_mul_f32_e32 v92, v131, v92
	v_cvt_pk_fp8_f32 v8, v9, v88
	v_mul_f32_e32 v9, 0xbfb8aa3b, v84
	v_mul_f32_e32 v88, v92, v91
	v_exp_f32_e32 v91, v9
	v_cvt_pk_fp8_f32 v8, v10, v11 op_sel:[0,0,1]
	v_mul_f32_e32 v11, 0xbfb8aa3b, v80
	v_exp_f32_e32 v11, v11
	v_add_f32_e32 v10, 1.0, v91
	v_rcp_f32_e32 v10, v10
	v_mov_b32_e32 v9, v189
	v_cvt_pk_fp8_f32 v9, v23, v89
	v_cmp_eq_u32_e32 vcc, 0, v22
	v_mul_f32_e32 v10, v84, v10
	v_mul_f32_e32 v23, v10, v76
	v_add_f32_e32 v10, 1.0, v11
	v_mul_f32_e32 v11, 0xbfb8aa3b, v85
	v_exp_f32_e32 v11, v11
	v_mul_f32_e32 v76, 0xbfb8aa3b, v81
	v_exp_f32_e32 v76, v76
	v_rcp_f32_e32 v10, v10
	v_add_f32_e32 v11, 1.0, v11
	v_rcp_f32_e32 v11, v11
	v_add_f32_e32 v76, 1.0, v76
	v_rcp_f32_e32 v76, v76
	v_mul_f32_e32 v10, v80, v10
; __device__ __forceinline__ float sigmoidf_(float x) { return __builtin_amdgcn_rcpf(1.f + __expf(-x)); }
; template <int MODE>
; __device__ __forceinline__ int moe_gemm(const Args& a, unsigned char* lds_g, int tid, int idx0) {
;     ...
;         if (MODE == 1) { unsigned char* HM = (unsigned char*)(a.ws + WS_HM) + (size_t)256 * ti * DE + 128 * nt + 64 * wn; const unsigned lo_ = (unsigned)((128 * hh + 64 * wr + efr) * DE + 16 * efq);
; #pragma unroll
;             for (int m = 0; m < 4; ++m) { v4u o16;
; #pragma unroll
;                 for (int n = 0; n < 4; n += 2) { float hv[8];
; #pragma unroll
;                     for (int r = 0; r < 4; ++r) { const float a1 = acc[m][n][r], a2 = acc[m][n + 1][r]; hv[r] = a1 * sigmoidf_(a1) * acc[m][n + 4][r]; hv[4 + r] = a2 * sigmoidf_(a2) * acc[m][n + 5][r]; }
;                     int w8a = __builtin_amdgcn_cvt_pk_fp8_f32(hv[0], hv[1], 0, false); w8a = __builtin_amdgcn_cvt_pk_fp8_f32(hv[2], hv[3], w8a, true);
;                     int w8b = __builtin_amdgcn_cvt_pk_fp8_f32(hv[4], hv[5], 0, false); w8b = __builtin_amdgcn_cvt_pk_fp8_f32(hv[6], hv[7], w8b, true);
;                     if (n == 0) { o16.x = (unsigned)w8a; o16.y = (unsigned)w8b; } else { o16.z = (unsigned)w8a; o16.w = (unsigned)w8b; } }
;                 { void* p_ = (void*)(HM + lo_ + 16 * m * DE); asm volatile("global_store_dwordx4 %0, %1, off sc1\n\ts_nop 1" :: "v"(p_), "v"(o16) : "memory"); } }
	v_mul_f32_e32 v72, v10, v72
	v_mul_f32_e32 v10, v85, v11
	v_mul_f32_e32 v11, v10, v77
	v_mul_f32_e32 v10, v81, v76
	v_mul_f32_e32 v76, 0xbfb8aa3b, v86
	v_exp_f32_e32 v76, v76
	v_mul_f32_e32 v77, 0xbfb8aa3b, v82
	v_exp_f32_e32 v77, v77
	v_mul_f32_e32 v73, v10, v73
	v_add_f32_e32 v10, 1.0, v76
	v_rcp_f32_e32 v10, v10
	v_add_f32_e32 v76, 1.0, v77
	v_mul_f32_e32 v77, 0xbfb8aa3b, v87
	v_rcp_f32_e32 v76, v76
	v_exp_f32_e32 v77, v77
	v_mul_f32_e32 v10, v86, v10
	v_mul_f32_e32 v78, v10, v78
	v_mul_f32_e32 v10, v82, v76
	v_add_f32_e32 v76, 1.0, v77
	v_rcp_f32_e32 v76, v76
	v_mul_f32_e32 v77, 0xbfb8aa3b, v83
	v_exp_f32_e32 v77, v77
	v_mul_f32_e32 v74, v10, v74
	v_mul_f32_e32 v10, v87, v76
	v_mul_f32_e32 v76, v10, v79
	v_add_f32_e32 v10, 1.0, v77
	v_rcp_f32_e32 v77, v10
	v_mov_b32_e32 v10, v189
	v_cvt_pk_fp8_f32 v10, v23, v11
	v_mov_b32_e32 v11, v189
	v_cvt_pk_fp8_f32 v11, v72, v73
	v_mul_f32_e32 v23, v83, v77
	v_mul_f32_e32 v23, v23, v75
	v_mul_f32_e32 v72, 0xbfb8aa3b, v64
	v_cvt_pk_fp8_f32 v11, v74, v23 op_sel:[0,0,1]
	v_mul_f32_e32 v23, 0xbfb8aa3b, v68
	v_exp_f32_e32 v23, v23
	v_exp_f32_e32 v74, v72
	v_cvt_pk_fp8_f32 v10, v78, v76 op_sel:[0,0,1]
	v_cvt_pk_fp8_f32 v9, v90, v88 op_sel:[0,0,1]
	v_add_f32_e32 v23, 1.0, v23
	v_rcp_f32_e32 v23, v23
	v_add_f32_e32 v74, 1.0, v74
	v_lshl_add_u64 v[72:73], v[20:21], 0, s[30:31]
	v_rcp_f32_e32 v74, v74
	global_store_dwordx4 v[72:73], v[8:11], off sc1
	s_nop 1
	v_mul_f32_e32 v10, 0xbfb8aa3b, v69
	v_exp_f32_e32 v10, v10
	v_mul_f32_e32 v11, 0xbfb8aa3b, v65
	v_exp_f32_e32 v11, v11
	v_mul_f32_e32 v8, v68, v23
	v_mul_f32_e32 v9, v8, v60
	v_mul_f32_e32 v8, v64, v74
	v_mul_f32_e32 v23, v8, v56
	v_add_f32_e32 v8, 1.0, v10
	v_rcp_f32_e32 v8, v8
	v_add_f32_e32 v10, 1.0, v11
	v_mul_f32_e32 v11, 0xbfb8aa3b, v70
	v_rcp_f32_e32 v10, v10
	v_exp_f32_e32 v11, v11
	v_mul_f32_e32 v8, v69, v8
	v_mul_f32_e32 v56, v8, v61
	v_mul_f32_e32 v8, v65, v10
	v_add_f32_e32 v10, 1.0, v11
	v_rcp_f32_e32 v10, v10
	v_mul_f32_e32 v11, 0xbfb8aa3b, v66
	v_exp_f32_e32 v11, v11
	v_mul_f32_e32 v57, v8, v57
	v_mul_f32_e32 v8, v70, v10
	v_mul_f32_e32 v10, v8, v62
	v_add_f32_e32 v8, 1.0, v11
	v_mul_f32_e32 v11, 0xbfb8aa3b, v71
	v_exp_f32_e32 v11, v11
	v_mul_f32_e32 v60, 0xbfb8aa3b, v67
	v_exp_f32_e32 v60, v60
	v_rcp_f32_e32 v8, v8
	v_add_f32_e32 v11, 1.0, v11
	v_rcp_f32_e32 v11, v11
	v_add_f32_e32 v60, 1.0, v60
	v_rcp_f32_e32 v60, v60
	v_mul_f32_e32 v8, v66, v8
	v_mul_f32_e32 v58, v8, v58
	v_mul_f32_e32 v8, v71, v11
	v_mul_f32_e32 v11, v8, v63
	v_mul_f32_e32 v8, v67, v60
	v_mul_f32_e32 v60, 0xbfb8aa3b, v52
	v_exp_f32_e32 v60, v60
	v_mul_f32_e32 v59, v8, v59
	v_mov_b32_e32 v8, v189
	v_cvt_pk_fp8_f32 v8, v9, v56
	v_mov_b32_e32 v9, v189
	v_mul_f32_e32 v56, 0xbfb8aa3b, v48
	v_cvt_pk_fp8_f32 v9, v23, v57
	v_add_f32_e32 v23, 1.0, v60
	v_exp_f32_e32 v56, v56
	v_rcp_f32_e32 v23, v23
	v_cvt_pk_fp8_f32 v8, v10, v11 op_sel:[0,0,1]
	v_cvt_pk_fp8_f32 v9, v58, v59 op_sel:[0,0,1]
	v_add_f32_e32 v11, 1.0, v56
	v_mul_f32_e32 v10, v52, v23
	v_rcp_f32_e32 v11, v11
	v_mul_f32_e32 v23, 0xbfb8aa3b, v53
	v_exp_f32_e32 v23, v23
	v_mul_f32_e32 v44, v10, v44
	v_mul_f32_e32 v10, v48, v11
	v_mul_f32_e32 v11, 0xbfb8aa3b, v49
	v_mul_f32_e32 v40, v10, v40
	v_add_f32_e32 v10, 1.0, v23
	v_exp_f32_e32 v11, v11
	v_mul_f32_e32 v23, 0xbfb8aa3b, v54
	v_exp_f32_e32 v23, v23
	v_rcp_f32_e32 v10, v10
	v_add_f32_e32 v11, 1.0, v11
	v_rcp_f32_e32 v11, v11
	v_add_f32_e32 v23, 1.0, v23
	v_rcp_f32_e32 v23, v23
	v_mul_f32_e32 v10, v53, v10
	v_mul_f32_e32 v45, v10, v45
	v_mul_f32_e32 v10, v49, v11
	v_mul_f32_e32 v11, 0xbfb8aa3b, v50
	v_mul_f32_e32 v41, v10, v41
	v_mul_f32_e32 v10, v54, v23
	v_exp_f32_e32 v11, v11
	v_mul_f32_e32 v23, 0xbfb8aa3b, v55
	v_exp_f32_e32 v23, v23
	v_mul_f32_e32 v46, v10, v46
	v_add_f32_e32 v10, 1.0, v11
	v_rcp_f32_e32 v10, v10
	v_add_f32_e32 v11, 1.0, v23
	v_mul_f32_e32 v23, 0xbfb8aa3b, v51
	v_exp_f32_e32 v23, v23
	v_mul_f32_e32 v10, v50, v10
	v_mul_f32_e32 v42, v10, v42
	v_rcp_f32_e32 v11, v11
	v_add_f32_e32 v10, 1.0, v23
	v_rcp_f32_e32 v23, v10
	v_mov_b32_e32 v10, v189
	v_cvt_pk_fp8_f32 v10, v44, v45
	v_mul_f32_e32 v44, 0xbfb8aa3b, v32
	v_mul_f32_e32 v23, v51, v23
	v_mul_f32_e32 v23, v23, v43
	v_mul_f32_e32 v43, 0xbfb8aa3b, v36
	v_exp_f32_e32 v43, v43
	v_mul_f32_e32 v11, v55, v11
	v_exp_f32_e32 v44, v44
	v_mul_f32_e32 v11, v11, v47
	v_cvt_pk_fp8_f32 v10, v46, v11 op_sel:[0,0,1]
	v_mov_b32_e32 v11, v189
	v_cvt_pk_fp8_f32 v11, v40, v41
	v_add_f32_e32 v40, 1.0, v43
	v_rcp_f32_e32 v40, v40
	v_add_f32_e32 v41, 1.0, v44
	v_rcp_f32_e32 v41, v41
	v_cvt_pk_fp8_f32 v11, v42, v23 op_sel:[0,0,1]
	v_mul_f32_e32 v23, v36, v40
	v_mul_f32_e32 v23, v23, v28
	v_mul_f32_e32 v28, v32, v41
	v_mul_f32_e32 v32, 0xbfb8aa3b, v37
	v_exp_f32_e32 v32, v32
	v_mul_f32_e32 v36, 0xbfb8aa3b, v33
	v_exp_f32_e32 v36, v36
	v_mul_f32_e32 v28, v28, v24
	v_add_f32_e32 v24, 1.0, v32
	v_rcp_f32_e32 v24, v24
	v_add_f32_e32 v32, 1.0, v36
	v_mul_f32_e32 v36, 0xbfb8aa3b, v38
	v_rcp_f32_e32 v32, v32
	v_exp_f32_e32 v36, v36
	v_mul_f32_e32 v24, v37, v24
	v_mul_f32_e32 v29, v24, v29
	v_mul_f32_e32 v24, v33, v32
	v_add_f32_e32 v32, 1.0, v36
	v_rcp_f32_e32 v32, v32
	v_mul_f32_e32 v33, 0xbfb8aa3b, v34
	v_mul_f32_e32 v36, v24, v25
	v_exp_f32_e32 v33, v33
	v_mul_f32_e32 v24, v38, v32
	v_mul_f32_e32 v25, v24, v30
	v_mul_f32_e32 v30, 0xbfb8aa3b, v39
	v_exp_f32_e32 v30, v30
	v_mul_f32_e32 v32, 0xbfb8aa3b, v35
	v_exp_f32_e32 v32, v32
	v_add_f32_e32 v24, 1.0, v33
	v_rcp_f32_e32 v24, v24
	v_add_f32_e32 v30, 1.0, v30
	v_rcp_f32_e32 v30, v30
	v_add_f32_e32 v32, 1.0, v32
	v_rcp_f32_e32 v32, v32
	v_mul_f32_e32 v24, v34, v24
	v_mul_f32_e32 v26, v24, v26
	v_mul_f32_e32 v24, v39, v30
	v_mul_f32_e32 v30, v24, v31
	v_mul_f32_e32 v31, v35, v32
; __device__ __forceinline__ float sigmoidf_(float x) { return __builtin_amdgcn_rcpf(1.f + __expf(-x)); }
; template <int MODE>
; __device__ __forceinline__ int moe_gemm(const Args& a, unsigned char* lds_g, int tid, int idx0) {
;     ...
;         if (MODE == 1) { unsigned char* HM = (unsigned char*)(a.ws + WS_HM) + (size_t)256 * ti * DE + 128 * nt + 64 * wn; const unsigned lo_ = (unsigned)((128 * hh + 64 * wr + efr) * DE + 16 * efq);
; #pragma unroll
;             for (int m = 0; m < 4; ++m) { v4u o16;
; #pragma unroll
;                 for (int n = 0; n < 4; n += 2) { float hv[8];
; #pragma unroll
;                     for (int r = 0; r < 4; ++r) { const float a1 = acc[m][n][r], a2 = acc[m][n + 1][r]; hv[r] = a1 * sigmoidf_(a1) * acc[m][n + 4][r]; hv[4 + r] = a2 * sigmoidf_(a2) * acc[m][n + 5][r]; }
;                     int w8a = __builtin_amdgcn_cvt_pk_fp8_f32(hv[0], hv[1], 0, false); w8a = __builtin_amdgcn_cvt_pk_fp8_f32(hv[2], hv[3], w8a, true);
;                     int w8b = __builtin_amdgcn_cvt_pk_fp8_f32(hv[4], hv[5], 0, false); w8b = __builtin_amdgcn_cvt_pk_fp8_f32(hv[6], hv[7], w8b, true);
;                     if (n == 0) { o16.x = (unsigned)w8a; o16.y = (unsigned)w8b; } else { o16.z = (unsigned)w8a; o16.w = (unsigned)w8b; } }
;                 { void* p_ = (void*)(HM + lo_ + 16 * m * DE); asm volatile("global_store_dwordx4 %0, %1, off sc1\n\ts_nop 1" :: "v"(p_), "v"(o16) : "memory"); } }
;             asm volatile("s_waitcnt vmcnt(0)" ::: "memory");
;             if (ln_ == 0) __hip_atomic_fetch_add((unsigned*)(a.ws + WS_CTL) + CW_TC + 64 * ti, 1u, __ATOMIC_RELAXED, __HIP_MEMORY_SCOPE_AGENT); }
	v_mov_b32_e32 v24, v189
	v_cvt_pk_fp8_f32 v24, v23, v29
	v_mul_f32_e32 v23, v31, v27
	v_mul_f32_e32 v27, 0xbfb8aa3b, v16
	v_exp_f32_e32 v27, v27
	v_cvt_pk_fp8_f32 v24, v25, v30 op_sel:[0,0,1]
	v_mov_b32_e32 v25, v189
	v_cvt_pk_fp8_f32 v25, v28, v36
	v_add_f32_e32 v27, 1.0, v27
	v_rcp_f32_e32 v27, v27
	v_mul_f32_e32 v28, 0xbfb8aa3b, v12
	v_exp_f32_e32 v28, v28
	v_cvt_pk_fp8_f32 v25, v26, v23 op_sel:[0,0,1]
	v_mul_f32_e32 v16, v16, v27
	v_mul_f32_e32 v4, v16, v4
	v_add_f32_e32 v16, 1.0, v28
	v_mul_f32_e32 v23, 0xbfb8aa3b, v17
	v_rcp_f32_e32 v16, v16
	v_exp_f32_e32 v23, v23
	v_mul_f32_e32 v26, 0xbfb8aa3b, v13
	v_exp_f32_e32 v26, v26
	v_mul_f32_e32 v12, v12, v16
	v_add_f32_e32 v16, 1.0, v23
	v_rcp_f32_e32 v16, v16
	v_add_f32_e32 v23, 1.0, v26
	v_rcp_f32_e32 v23, v23
	v_mul_f32_e32 v0, v12, v0
	v_mul_f32_e32 v12, v17, v16
	v_mul_f32_e32 v5, v12, v5
	v_mul_f32_e32 v12, v13, v23
	v_mul_f32_e32 v13, 0xbfb8aa3b, v18
	v_exp_f32_e32 v13, v13
	v_mul_f32_e32 v16, 0xbfb8aa3b, v14
	v_exp_f32_e32 v16, v16
	v_mul_f32_e32 v1, v12, v1
	v_add_f32_e32 v12, 1.0, v13
	v_rcp_f32_e32 v12, v12
	v_add_f32_e32 v13, 1.0, v16
	v_mul_f32_e32 v16, 0xbfb8aa3b, v19
	v_rcp_f32_e32 v13, v13
	v_exp_f32_e32 v16, v16
	v_mul_f32_e32 v12, v18, v12
	v_mul_f32_e32 v6, v12, v6
	v_mul_f32_e32 v12, v14, v13
	v_add_f32_e32 v13, 1.0, v16
	v_rcp_f32_e32 v13, v13
	v_mul_f32_e32 v14, 0xbfb8aa3b, v15
	v_exp_f32_e32 v14, v14
	v_mul_f32_e32 v2, v12, v2
	v_mul_f32_e32 v12, v19, v13
	v_mul_f32_e32 v7, v12, v7
	v_add_f32_e32 v12, 1.0, v14
	v_rcp_f32_e32 v12, v12
	v_mov_b32_e32 v27, v189
	v_mov_b32_e32 v26, v189
	v_cvt_pk_fp8_f32 v27, v0, v1
	v_cvt_pk_fp8_f32 v26, v4, v5
	v_mul_f32_e32 v0, v15, v12
	v_mul_f32_e32 v0, v0, v3
	v_cvt_pk_fp8_f32 v27, v2, v0 op_sel:[0,0,1]
	v_lshl_add_u64 v[0:1], v[20:21], 0, s[34:35]
	global_store_dwordx4 v[0:1], v[8:11], off sc1
	s_nop 1
	v_cvt_pk_fp8_f32 v26, v6, v7 op_sel:[0,0,1]
	v_lshl_add_u64 v[0:1], v[20:21], 0, s[36:37]
	global_store_dwordx4 v[0:1], v[24:27], off sc1
	s_nop 1
	s_waitcnt vmcnt(0)
	s_and_saveexec_b64 s[6:7], vcc
	s_cbranch_execz .LBB0_1169
	s_mov_b64 s[16:17], exec
	v_mbcnt_lo_u32_b32 v0, s16, 0
	v_mbcnt_hi_u32_b32 v0, s17, v0
	v_cmp_eq_u32_e32 vcc, 0, v0
	s_and_b64 s[20:21], exec, vcc
	s_mov_b64 exec, s[20:21]
	s_cbranch_execz .LBB0_1169
	s_lshl_b32 s26, s38, 6
	s_lshl_b64 s[20:21], s[26:27], 2
	s_add_u32 s20, s40, s20
	s_addc_u32 s21, s41, s21
	s_bcnt1_i32_b64 s16, s[16:17]
	v_mov_b32_e32 v0, s16
	global_atomic_add v189, v0, s[20:21]
	s_branch .LBB0_1169
.Lnm1_head:
	s_waitcnt lgkmcnt(0)
	s_barrier
	s_nop 0
	s_nop 0
	s_nop 0
	s_nop 0
	s_nop 0
	s_nop 0
	s_nop 0
	s_nop 0
	s_nop 0
	s_nop 0
	s_nop 0
	s_nop 0
	s_min_u32 s22, s65, 28
	s_add_i32 s39, s65, 2
	s_add_i32 s22, s22, 3
	s_cmp_lt_u32 s65, 30
	s_cselect_b32 s73, s26, 0x7c0
	s_lshl_b32 s69, s22, 18
	s_lshl_b32 s75, s73, 12
	s_lshl_b32 s74, s22, 6
	s_addk_i32 s26, 0x80
	s_or_b32 s68, s69, 0x10000
	s_or_b32 s67, s69, 0x20000
	s_or_b32 s66, s69, 0x30000
	s_or_b32 s72, s75, 0x10000
	s_or_b32 s71, s75, 0x20000
	s_or_b32 s70, s75, 0x30000
	s_cmp_gt_u32 s65, 29
	buffer_load_dwordx4 v[168:171], v192, s[76:79], s75 offen
	s_waitcnt vmcnt(8)
	v_cvt_pk_bf16_f32 v214, v124, v125
	v_cvt_pk_bf16_f32 v215, v126, v127
	v_add_u32_e32 v242, 0x18400, v194
	s_waitcnt lgkmcnt(2)
	s_nop 0
	ds_write_b64 v242, v[214:215]
	v_cvt_pk_f32_fp8_e32 v[214:215], v21
	v_cvt_pk_f32_fp8_e32 v[216:217], v23
	v_cvt_pk_f32_fp8_e32 v[160:161], v20
	v_cvt_pk_f32_fp8_sdwa v[162:163], v20 src0_sel:WORD_1
	v_cvt_pk_f32_fp8_sdwa v[20:21], v21 src0_sel:WORD_1
	v_cvt_pk_f32_fp8_sdwa v[218:219], v23 src0_sel:WORD_1
	v_cvt_pk_bf16_f32 v160, v160, v161
	v_cvt_pk_bf16_f32 v161, v162, v163
	v_cvt_pk_bf16_f32 v162, v214, v215
	v_cvt_pk_f32_fp8_e32 v[214:215], v22
	v_cvt_pk_bf16_f32 v163, v20, v21
	s_nop 0
	ds_write_b128 v193, v[160:163] offset:32768
	v_cvt_pk_bf16_f32 v20, v214, v215
	v_cvt_pk_f32_fp8_sdwa v[214:215], v22 src0_sel:WORD_1
	s_nop 0
	v_cvt_pk_bf16_f32 v22, v216, v217
	v_cvt_pk_bf16_f32 v23, v218, v219
	v_cvt_pk_bf16_f32 v21, v214, v215
	s_nop 0
	ds_write_b128 v193, v[20:23] offset:32784
	s_nop 0
	s_nop 0
	s_nop 0
	s_nop 0
	s_nop 0
	s_nop 0
	s_nop 0
	s_nop 0
	s_mov_b32 s22, s78
	s_mov_b32 s23, s79
	buffer_load_dwordx4 v[32:35], v192, s[20:23], s75 offen
	v_cvt_pk_f32_fp8_e32 v[22:23], v8
	v_cvt_pk_f32_fp8_sdwa v[36:37], v8 src0_sel:WORD_1
	s_waitcnt vmcnt(7)
	v_cvt_pk_bf16_f32 v20, v120, v121
	v_cvt_pk_bf16_f32 v21, v122, v123
	ds_write_b64 v242, v[20:21] offset:128
	v_cvt_pk_bf16_f32 v20, v22, v23
	v_cvt_pk_f32_fp8_e32 v[22:23], v9
	v_cvt_pk_f32_fp8_sdwa v[8:9], v9 src0_sel:WORD_1
	v_cvt_pk_bf16_f32 v21, v36, v37
	v_cvt_pk_f32_fp8_e32 v[36:37], v10
	v_cvt_pk_bf16_f32 v22, v22, v23
	v_cvt_pk_bf16_f32 v23, v8, v9
	ds_write_b128 v193, v[20:23] offset:49152
	v_cvt_pk_bf16_f32 v8, v36, v37
	v_cvt_pk_f32_fp8_sdwa v[20:21], v10 src0_sel:WORD_1
	v_cvt_pk_f32_fp8_e32 v[22:23], v11
	v_cvt_pk_f32_fp8_sdwa v[36:37], v11 src0_sel:WORD_1
	s_waitcnt lgkmcnt(10)
	s_nop 0
	v_cvt_pk_bf16_f32 v9, v20, v21
	v_cvt_pk_bf16_f32 v10, v22, v23
	v_cvt_pk_bf16_f32 v11, v36, v37
	s_waitcnt lgkmcnt(9)
	s_nop 0
	ds_write_b128 v193, v[8:11] offset:49168
	s_nop 0
	s_nop 0
	s_nop 0
	s_nop 0
	s_nop 0
	s_nop 0
	s_nop 0
	s_nop 0
	s_nop 0
	s_nop 0
	s_nop 0
	s_nop 0
	s_nop 0
	s_nop 0
	buffer_load_dwordx4 v[12:15], v192, s[76:79], s72 offen
	buffer_load_dwordx4 v[48:51], v188, s[4:7], s73 offen
	buffer_load_dwordx4 v[20:23], v188, s[4:7], s74 offen
	buffer_load_dwordx4 v[36:39], v191, s[4:7], s73 offen
	buffer_load_dwordx4 v[8:11], v191, s[4:7], s74 offen
	s_waitcnt lgkmcnt(13)
	s_nop 0
	v_cvt_pk_bf16_f32 v16, v92, v93
	v_cvt_pk_bf16_f32 v17, v94, v95
	ds_write_b64 v242, v[16:17] offset:8448
	s_waitcnt lgkmcnt(12)
; #define MG_BAR() do { asm volatile("s_waitcnt lgkmcnt(0)" ::: "memory"); __builtin_amdgcn_s_barrier(); asm volatile("" ::: "memory"); } while (0)
; #define MH_LDA(te_, to_) do { ra[0] = __builtin_amdgcn_raw_buffer_load_b128(rsA, aofs[0], 64 * (te_), 0); ra[1] = __builtin_amdgcn_raw_buffer_load_b128(rsA, aofs[1], 64 * (te_), 0); \
;             ra[2] = __builtin_amdgcn_raw_buffer_load_b128(rsA, aofs[0], 64 * (to_), 0); ra[3] = __builtin_amdgcn_raw_buffer_load_b128(rsA, aofs[1], 64 * (to_), 0); } while (0)
; template <int MODE>
; __device__ __forceinline__ int moe_gemm(const Args& a, unsigned char* lds_g, int tid, int idx0) {
;     ...
;             for (int t = 0; t < NT; t += 2) {
;                 const int t2 = (t + 2 < NT) ? t + 2 : NT - 1, t3 = (t + 3 < NT) ? t + 3 : NT - 1;
;                 MG_BAR();
;                 MH_MMAI(0, 1, 2, t2, MH_LDA(t2, t3));
;                 MG_BAR();
;                 MH_MMAI(1, 0, 0, t3, (void)0);
;             }
	s_nop 0
	s_nop 0
	s_nop 0
	s_nop 0
	s_nop 0
	s_nop 0
	s_nop 0
	s_nop 2
	s_nop 0
	s_nop 0
	s_nop 0
	s_nop 0
	buffer_load_dwordx4 v[16:19], v192, s[20:23], s72 offen
	s_waitcnt lgkmcnt(7)
	s_nop 0
	s_waitcnt lgkmcnt(5)
	s_nop 0
	s_nop 0
	s_nop 0
	s_nop 0
	s_nop 0
	s_nop 0
	s_waitcnt vmcnt(12)
	s_nop 1
	v_cvt_pk_bf16_f32 v4, v100, v101
	v_cvt_pk_bf16_f32 v5, v102, v103
	s_nop 0
	ds_write_b64 v242, v[4:5] offset:8576
	s_nop 0
	s_nop 0
	s_nop 0
	s_nop 0
	buffer_load_dwordx4 v[0:3], v192, s[76:79], s71 offen
	s_waitcnt lgkmcnt(7)
	s_nop 0
	s_waitcnt vmcnt(12)
	v_cvt_pk_bf16_f32 v4, v104, v105
	v_cvt_pk_bf16_f32 v5, v106, v107
	ds_write_b64 v242, v[4:5] offset:16896
	s_nop 0
	s_waitcnt lgkmcnt(6)
	s_nop 0
	s_nop 0
	s_nop 0
	s_nop 0
	s_nop 0
	s_nop 0
	s_nop 2
	s_nop 0
	s_nop 0
	s_nop 0
	s_nop 0
	buffer_load_dwordx4 v[4:7], v192, s[20:23], s71 offen
	s_waitcnt lgkmcnt(7)
	s_nop 0
	s_waitcnt vmcnt(11)
	v_cvt_pk_bf16_f32 v24, v112, v113
	v_cvt_pk_bf16_f32 v25, v114, v115
	ds_write_b64 v242, v[24:25] offset:17024
	s_nop 0
	s_waitcnt lgkmcnt(6)
	s_nop 0
	s_nop 0
	s_nop 0
	s_nop 0
	s_nop 0
	s_nop 0
	s_nop 1
	s_nop 0
	s_nop 0
	s_nop 0
	s_nop 0
	buffer_load_dwordx4 v[24:27], v192, s[76:79], s70 offen
	v_cvt_pk_bf16_f32 v108, v108, v109
	v_cvt_pk_bf16_f32 v109, v110, v111
	s_waitcnt lgkmcnt(7)
	s_nop 0
	ds_write_b64 v242, v[108:109] offset:25344
	s_waitcnt lgkmcnt(6)
	s_nop 0
	s_nop 0
	s_nop 0
	s_nop 0
	s_nop 0
	s_nop 0
	s_nop 0
	buffer_load_dwordx4 v[172:175], v192, s[20:23], s70 offen
	s_waitcnt lgkmcnt(3)
	s_nop 0
	s_waitcnt vmcnt(12)
	v_cvt_pk_bf16_f32 v92, v116, v117
	v_cvt_pk_bf16_f32 v93, v118, v119
	ds_write_b64 v242, v[92:93] offset:25472
	s_waitcnt lgkmcnt(2)
	s_nop 0
	s_nop 0
	s_nop 0
	s_nop 0
	s_nop 0
	s_nop 0
	s_nop 0
	s_waitcnt lgkmcnt(0)
	s_barrier
	s_nop 0
	s_nop 0
	s_nop 0
	s_nop 0
	s_nop 0
	s_nop 0
	s_nop 0
	s_nop 0
	s_nop 0
	s_nop 0
	s_nop 0
	s_nop 0
	s_nop 0
	buffer_load_dwordx4 v[124:127], v192, s[76:79], s69 offen
	s_waitcnt vmcnt(12)
	v_cvt_pk_bf16_f32 v222, v168, v169
	v_cvt_pk_bf16_f32 v223, v170, v171
	s_waitcnt lgkmcnt(2)
	s_nop 0
	ds_write_b64 v195, v[222:223]
	s_waitcnt vmcnt(9)
	v_cvt_pk_f32_fp8_e32 v[222:223], v49
	v_cvt_pk_f32_fp8_e32 v[224:225], v51
	v_cvt_pk_f32_fp8_e32 v[184:185], v48
	v_cvt_pk_f32_fp8_sdwa v[186:187], v48 src0_sel:WORD_1
	v_cvt_pk_f32_fp8_sdwa v[48:49], v49 src0_sel:WORD_1
	v_cvt_pk_f32_fp8_sdwa v[226:227], v51 src0_sel:WORD_1
	v_cvt_pk_bf16_f32 v184, v184, v185
	v_cvt_pk_bf16_f32 v185, v186, v187
	v_cvt_pk_bf16_f32 v186, v222, v223
	v_cvt_pk_f32_fp8_e32 v[222:223], v50
	v_cvt_pk_bf16_f32 v187, v48, v49
	v_cvt_pk_bf16_f32 v51, v226, v227
	s_nop 0
	v_cvt_pk_bf16_f32 v48, v222, v223
	v_cvt_pk_f32_fp8_sdwa v[222:223], v50 src0_sel:WORD_1
	v_cvt_pk_bf16_f32 v50, v224, v225
	s_nop 0
	ds_write_b128 v193, v[184:187]
	v_cvt_pk_bf16_f32 v49, v222, v223
	ds_write_b128 v193, v[48:51] offset:16
	s_nop 0
	s_nop 0
	s_nop 0
	s_nop 0
	s_nop 0
	s_nop 1
	s_nop 0
	s_nop 0
	s_nop 0
	s_nop 0
	buffer_load_dwordx4 v[120:123], v192, s[20:23], s69 offen
	v_cvt_pk_bf16_f32 v32, v32, v33
	v_cvt_pk_bf16_f32 v33, v34, v35
	s_waitcnt vmcnt(8)
	v_cvt_pk_f32_fp8_e32 v[34:35], v36
	ds_write_b64 v195, v[32:33] offset:128
	v_cvt_pk_f32_fp8_sdwa v[92:93], v36 src0_sel:WORD_1
	s_waitcnt lgkmcnt(9)
	s_nop 0
	v_cvt_pk_bf16_f32 v32, v34, v35
	v_cvt_pk_f32_fp8_e32 v[34:35], v37
	v_cvt_pk_f32_fp8_sdwa v[36:37], v37 src0_sel:WORD_1
	v_cvt_pk_bf16_f32 v33, v92, v93
	v_cvt_pk_f32_fp8_e32 v[92:93], v38
	v_cvt_pk_bf16_f32 v34, v34, v35
	v_cvt_pk_bf16_f32 v35, v36, v37
	ds_write_b128 v193, v[32:35] offset:16384
	v_cvt_pk_f32_fp8_sdwa v[34:35], v38 src0_sel:WORD_1
	v_cvt_pk_f32_fp8_e32 v[36:37], v39
	v_cvt_pk_f32_fp8_sdwa v[38:39], v39 src0_sel:WORD_1
	s_nop 0
	v_cvt_pk_bf16_f32 v32, v92, v93
	v_cvt_pk_bf16_f32 v33, v34, v35
	v_cvt_pk_bf16_f32 v34, v36, v37
	s_waitcnt lgkmcnt(9)
	s_nop 0
	v_cvt_pk_bf16_f32 v35, v38, v39
	ds_write_b128 v193, v[32:35] offset:16400
	s_nop 0
	s_nop 0
	s_nop 0
	s_nop 0
	s_nop 0
	s_nop 0
	s_nop 0
	s_nop 0
	s_nop 0
	s_nop 0
	s_nop 0
	s_nop 0
	s_nop 0
	buffer_load_dwordx4 v[92:95], v192, s[76:79], s68 offen
	s_waitcnt lgkmcnt(13)
	s_nop 0
	v_cvt_pk_bf16_f32 v12, v12, v13
	v_cvt_pk_bf16_f32 v13, v14, v15
	ds_write_b64 v195, v[12:13] offset:8448
	s_waitcnt lgkmcnt(12)
	s_nop 0
	s_nop 0
	s_nop 0
	s_nop 0
	s_nop 0
	s_nop 0
	s_nop 0
	s_nop 0
	s_nop 0
	s_nop 0
	s_nop 0
	s_nop 0
	s_waitcnt lgkmcnt(7)
	s_nop 0
	s_waitcnt vmcnt(7)
	v_cvt_pk_bf16_f32 v16, v16, v17
	v_cvt_pk_bf16_f32 v17, v18, v19
	ds_write_b64 v195, v[16:17] offset:8576
	s_waitcnt lgkmcnt(6)
	s_nop 0
	buffer_load_dwordx4 v[100:103], v192, s[20:23], s68 offen
	s_nop 0
	s_nop 0
	s_nop 0
	s_nop 0
	s_nop 0
	s_nop 0
	s_nop 0
	s_nop 0
	s_nop 0
	s_nop 0
	s_nop 0
	buffer_load_dwordx4 v[104:107], v192, s[76:79], s67 offen
	s_waitcnt lgkmcnt(7)
	s_nop 0
	s_waitcnt vmcnt(8)
	v_cvt_pk_bf16_f32 v0, v0, v1
	v_cvt_pk_bf16_f32 v1, v2, v3
	ds_write_b64 v195, v[0:1] offset:16896
	s_waitcnt lgkmcnt(6)
	s_nop 0
	s_nop 0
	s_nop 0
	s_nop 0
	s_nop 0
	s_nop 0
	s_nop 0
	s_nop 0
	s_nop 0
	s_nop 0
	s_nop 0
	buffer_load_dwordx4 v[112:115], v192, s[20:23], s67 offen
	s_waitcnt lgkmcnt(7)
	s_nop 0
	s_waitcnt vmcnt(8)
	v_cvt_pk_bf16_f32 v4, v4, v5
	v_cvt_pk_bf16_f32 v5, v6, v7
	ds_write_b64 v195, v[4:5] offset:17024
	s_waitcnt lgkmcnt(6)
	s_nop 0
	s_nop 0
	s_nop 0
	s_nop 0
	s_nop 0
	s_nop 0
	s_nop 0
	s_nop 0
	s_nop 0
	s_nop 0
	s_nop 0
	buffer_load_dwordx4 v[108:111], v192, s[76:79], s66 offen
	s_waitcnt lgkmcnt(7)
	s_nop 0
	s_waitcnt lgkmcnt(5)
	s_nop 0
	s_nop 0
	s_nop 0
	s_nop 0
	s_nop 0
	s_nop 0
	s_waitcnt vmcnt(8)
	v_cvt_pk_bf16_f32 v0, v24, v25
	v_cvt_pk_bf16_f32 v1, v26, v27
	ds_write_b64 v195, v[0:1] offset:25344
	s_nop 0
	buffer_load_dwordx4 v[116:119], v192, s[20:23], s66 offen
	s_waitcnt vmcnt(8)
	v_cvt_pk_bf16_f32 v0, v172, v173
	v_cvt_pk_bf16_f32 v1, v174, v175
	s_waitcnt lgkmcnt(3)
	s_nop 0
	ds_write_b64 v195, v[0:1] offset:25472
	s_waitcnt lgkmcnt(2)
	s_nop 0
	s_nop 0
	s_nop 0
	s_nop 0
	s_nop 0
	s_nop 0
	s_nop 0
	s_mov_b32 s65, s39
	s_cbranch_scc0 .Lnm1_head
	s_branch .Lnm1_exit

; __device__ __forceinline__ unsigned xb_ld(unsigned* p)              { return __hip_atomic_load(p, __ATOMIC_RELAXED, __HIP_MEMORY_SCOPE_AGENT); }
; __device__ __forceinline__ unsigned xb_add(unsigned* p, unsigned v) { return __hip_atomic_fetch_add(p, v, __ATOMIC_RELAXED, __HIP_MEMORY_SCOPE_AGENT); }
; #define XB_SPIN(cond, bar) do { unsigned _sp = 0; while (cond) { __builtin_amdgcn_s_sleep(1); \
;     if ((++_sp & 255u) == 0u) { if (xb_ld(&(bar)[XB_TMO])) break; if (_sp > XB_SPIN_CAP) { atomicAdd(&(bar)[XB_TMO], 1u); break; } } } } while (0)
; __device__ __forceinline__ void xcd_barrier(const XcdBarrier& b, int tid) {
;     ...
;         const unsigned old = xb_add(&bar[XB_XSUB(b.x)], 1u);
;         const unsigned gen = old / nloc;
;         if (old + 1u == (gen + 1u) * nloc) {
;             __builtin_amdgcn_fence(__ATOMIC_RELEASE, "agent");
;             asm volatile("s_waitcnt vmcnt(0)" ::: "memory");
;             const unsigned og = xb_add(&bar[XB_TOP], 1u);
;             const unsigned tg = og / nx;
;             if (og + 1u == (tg + 1u) * nx) xb_add(&bar[XB_TOPGEN], 1u);
;             else XB_SPIN(xb_ld(&bar[XB_TOPGEN]) == tg, bar);
;             __builtin_amdgcn_fence(__ATOMIC_ACQUIRE, "agent");
;             xb_add(&bar[XB_XGEN(b.x)], 1u);
;             asm volatile("s_waitcnt vmcnt(0)" ::: "memory");
;         } else {
;             XB_SPIN(xb_ld(&bar[XB_XGEN(b.x)]) == gen, bar);
;             __builtin_amdgcn_fence(__ATOMIC_ACQUIRE, "agent");
;             asm volatile("s_waitcnt vmcnt(0)" ::: "memory");
;         }
.LBB0_1232:
	v_readlane_b32 s2, v249, 2
	s_lshl_b32 s2, s2, 8
	v_readlane_b32 s6, v249, 3
	v_readlane_b32 s7, v249, 4
	s_add_u32 s6, s6, s2
	s_addc_u32 s7, s7, 0
	v_mov_b32_e32 v1, 0x1000
	v_mov_b32_e32 v3, 1
	v_sub_u32_e32 v4, 0, v2
	global_atomic_add v3, v1, v3, s[6:7] offset:1024 sc0
	v_cvt_f32_u32_e32 v1, v2
	v_rcp_iflag_f32_e32 v1, v1
	s_nop 0
	v_mul_f32_e32 v1, 0x4f7ffffe, v1
	v_cvt_u32_f32_e32 v1, v1
	v_mul_lo_u32 v4, v4, v1
	v_mul_hi_u32 v4, v1, v4
	v_add_u32_e32 v1, v1, v4
	s_waitcnt vmcnt(0)
	v_mul_hi_u32 v1, v3, v1
	v_mul_lo_u32 v4, v1, v2
	v_sub_u32_e32 v4, v3, v4
	v_add_u32_e32 v5, 1, v1
	v_cmp_ge_u32_e32 vcc, v4, v2
	v_add_u32_e32 v3, 1, v3
	s_nop 0
	v_cndmask_b32_e32 v1, v1, v5, vcc
	v_sub_u32_e32 v5, v4, v2
	v_cndmask_b32_e32 v4, v4, v5, vcc
	v_add_u32_e32 v5, 1, v1
	v_cmp_ge_u32_e32 vcc, v4, v2
	s_nop 1
	v_cndmask_b32_e32 v1, v1, v5, vcc
	v_mul_lo_u32 v4, v2, v1
	v_add_u32_e32 v2, v4, v2
	v_cmp_ne_u32_e32 vcc, v3, v2
	s_and_saveexec_b64 s[2:3], vcc
	s_xor_b64 s[8:9], exec, s[2:3]
	s_cbranch_execz .LBB0_1246
	s_waitcnt lgkmcnt(0)
	buffer_inv sc1
	v_mov_b32_e32 v0, 0x7100
	global_load_dword v0, v0, s[84:85] offset:1024 sc1
	s_add_u32 s18, s84, 0x7500
	s_addc_u32 s19, s85, 0
	s_waitcnt vmcnt(0)
	v_cmp_eq_u32_e32 vcc, v0, v1
	s_and_saveexec_b64 s[10:11], vcc
	s_cbranch_execz .LBB0_1245
	s_add_u32 s16, s84, 0x4200
	s_addc_u32 s17, s85, 0
	s_mov_b32 s2, 1
	s_mov_b64 s[20:21], 0
	v_mov_b32_e32 v0, 0
	s_branch .LBB0_1236

; __device__ __forceinline__ unsigned xb_ld(unsigned* p)              { return __hip_atomic_load(p, __ATOMIC_RELAXED, __HIP_MEMORY_SCOPE_AGENT); }
; __device__ __forceinline__ unsigned xb_add(unsigned* p, unsigned v) { return __hip_atomic_fetch_add(p, v, __ATOMIC_RELAXED, __HIP_MEMORY_SCOPE_AGENT); }
; #define XB_SPIN(cond, bar) do { unsigned _sp = 0; while (cond) { __builtin_amdgcn_s_sleep(1); \
;     if ((++_sp & 255u) == 0u) { if (xb_ld(&(bar)[XB_TMO])) break; if (_sp > XB_SPIN_CAP) { atomicAdd(&(bar)[XB_TMO], 1u); break; } } } } while (0)
; __device__ __forceinline__ void xcd_barrier(const XcdBarrier& b, int tid) {
;     ...
;         const unsigned old = xb_add(&bar[XB_XSUB(b.x)], 1u);
;         const unsigned gen = old / nloc;
;         if (old + 1u == (gen + 1u) * nloc) {
;             __builtin_amdgcn_fence(__ATOMIC_RELEASE, "agent");
;             asm volatile("s_waitcnt vmcnt(0)" ::: "memory");
;             const unsigned og = xb_add(&bar[XB_TOP], 1u);
;             const unsigned tg = og / nx;
;             if (og + 1u == (tg + 1u) * nx) xb_add(&bar[XB_TOPGEN], 1u);
;             else XB_SPIN(xb_ld(&bar[XB_TOPGEN]) == tg, bar);
;             __builtin_amdgcn_fence(__ATOMIC_ACQUIRE, "agent");
;             xb_add(&bar[XB_XGEN(b.x)], 1u);
;             asm volatile("s_waitcnt vmcnt(0)" ::: "memory");
;         } else {
;             XB_SPIN(xb_ld(&bar[XB_XGEN(b.x)]) == gen, bar);
;             __builtin_amdgcn_fence(__ATOMIC_ACQUIRE, "agent");
;             asm volatile("s_waitcnt vmcnt(0)" ::: "memory");
;         }
.LBB0_1298:
	v_readlane_b32 s2, v249, 2
	s_lshl_b32 s2, s2, 8
	v_readlane_b32 s4, v249, 3
	v_readlane_b32 s5, v249, 4
	s_add_u32 s2, s4, s2
	s_addc_u32 s3, s5, 0
	v_mov_b32_e32 v1, 0x1000
	v_mov_b32_e32 v3, 1
	global_atomic_add v3, v1, v3, s[2:3] offset:1024 sc0
	v_cvt_f32_u32_e32 v1, v2
	v_sub_u32_e32 v4, 0, v2
	v_rcp_iflag_f32_e32 v1, v1
	s_nop 0
	v_mul_f32_e32 v1, 0x4f7ffffe, v1
	v_cvt_u32_f32_e32 v1, v1
	v_mul_lo_u32 v4, v4, v1
	v_mul_hi_u32 v4, v1, v4
	v_add_u32_e32 v1, v1, v4
	s_waitcnt vmcnt(0)
	v_mul_hi_u32 v1, v3, v1
	v_mul_lo_u32 v4, v1, v2
	v_sub_u32_e32 v4, v3, v4
	v_add_u32_e32 v5, 1, v1
	v_cmp_ge_u32_e32 vcc, v4, v2
	v_add_u32_e32 v3, 1, v3
	s_nop 0
	v_cndmask_b32_e32 v1, v1, v5, vcc
	v_sub_u32_e32 v5, v4, v2
	v_cndmask_b32_e32 v4, v4, v5, vcc
	v_add_u32_e32 v5, 1, v1
	v_cmp_ge_u32_e32 vcc, v4, v2
	s_nop 1
	v_cndmask_b32_e32 v1, v1, v5, vcc
	v_mul_lo_u32 v4, v2, v1
	v_add_u32_e32 v2, v4, v2
	v_cmp_ne_u32_e32 vcc, v3, v2
	s_and_saveexec_b64 s[4:5], vcc
	s_xor_b64 s[4:5], exec, s[4:5]
	s_cbranch_execz .LBB0_1312
	s_waitcnt lgkmcnt(0)
	buffer_inv sc1
	v_mov_b32_e32 v0, 0x7100
	global_load_dword v0, v0, s[84:85] offset:1024 sc1
	s_add_u32 s10, s84, 0x7500
	s_addc_u32 s11, s85, 0
	s_waitcnt vmcnt(0)
	v_cmp_eq_u32_e32 vcc, v0, v1
	s_and_saveexec_b64 s[6:7], vcc
	s_cbranch_execz .LBB0_1311
	s_add_u32 s8, s84, 0x4200
	s_addc_u32 s9, s85, 0
	s_mov_b32 s22, 1
	s_mov_b64 s[12:13], 0
	v_mov_b32_e32 v0, 0
	s_branch .LBB0_1302
